# GEMM K-loops: setprio moved outside the barrier-to-barrier MFMA window
# baseline (speedup 1.0000x reference)
; #define PG8_STAGE(bufoff, gbase, voff) do { _Pragma("unroll") for (int _i = 0; _i < 2; ++_i) \
;         __builtin_amdgcn_global_load_lds((const unsigned*)((const char*)(gbase) + (voff)[_i]), (PG8_LAS unsigned*)(lds + (bufoff) + ldsw + _i * 8192), 16, 0, 0); } while (0)
; #define PG8_LDA(dst, b, h) do { _Pragma("unroll") for (int m = 0; m < 4; ++m) _Pragma("unroll") for (int k = 0; k < 2; ++k) dst[m][k] = *(const PG8_LAS bf16x8*)(lds + PG8_SA(b, h) + aoff + m * 2048 + k * 1024); } while (0)
; #define PG8_LDB(dst, b, h) do { _Pragma("unroll") for (int n = 0; n < 2; ++n) _Pragma("unroll") for (int k = 0; k < 2; ++k) dst[n][k] = *(const PG8_LAS bf16x8*)(lds + PG8_SB(b, h) + boff + n * 2048 + k * 1024); } while (0)
; #define PG8_MMA(ai, bj, At, Bt) do { __builtin_amdgcn_s_setprio(1); _Pragma("unroll") for (int m = 0; m < 4; ++m) _Pragma("unroll") for (int n = 0; n < 2; ++n) _Pragma("unroll") for (int k = 0; k < 2; ++k) \
;         acc[ai][bj][m][n] = __builtin_amdgcn_mfma_f32_16x16x32_bf16(Bt[n][k], At[m][k], acc[ai][bj][m][n], 0, 0, 0); __builtin_amdgcn_s_setprio(0); } while (0)
; #define PG8_WAIT_V(n) asm volatile("s_waitcnt vmcnt(" #n ")" ::: "memory")
; #define PG8_WAIT_L(n) asm volatile("s_waitcnt lgkmcnt(" #n ")" ::: "memory")
; template <class Epi, class Sched, bool ALIGN_EPI = false, bool SP2 = false>
; __device__ __forceinline__ void gemm_phase(PG8_LAS unsigned char* lds, const Gemm g, const Sched& S, const Epi& E) {
;     ...
;             const bool last = (t == nt - 2);
;             const char* a1 = cA + (size_t)(t + 1) * kstep;
;             const char* a2 = last ? nA : cA + (size_t)(t + 2) * kstep; const char* b2 = last ? nB : cB + (size_t)(t + 2) * kstep;
;             const char* a3 = a2 + kstep; const char* b3 = b2 + kstep;
;             if (last && has_next) S.a_ready(nxt);
;             if constexpr (SP2) {
;             PG8_LDB(B0, 0, 0); PG8_LDB(B1, 0, 1); PG8_SCHED; PG8_LDA(At, 0, 0); PG8_STAGEA(PG8_SA(1, 1), a1, 1, false);
;             PG8_WAIT_V(8); PG8_WAIT_L(0); PG8_BAR; PG8_MMA(0, 0, At, B0); PG8_MMA(0, 1, At, B1); PG8_BAR; PG8_SCHED;
;             PG8_LDA(At, 0, 1); PG8_STAGE(PG8_SB(0, 0), b2, voffB); PG8_STAGE(PG8_SB(0, 1), b2 + hstep, voffB); PG8_STAGEA(PG8_SA(0, 0), a2, 0, last);
;             PG8_WAIT_V(8); PG8_WAIT_L(0); PG8_BAR; PG8_MMA(1, 0, At, B0); PG8_MMA(1, 1, At, B1); PG8_BAR; PG8_SCHED;
.LBB0_110:
	v_add_u32_e32 v142, s79, v170
	v_add_u32_e32 v175, s80, v170
	ds_read_b128 v[130:133], v142
	ds_read_b128 v[134:137], v142 offset:1024
	ds_read_b128 v[138:141], v142 offset:2048
	ds_read_b128 v[142:145], v142 offset:3072
	ds_read_b128 v[162:165], v175
	ds_read_b128 v[166:169], v175 offset:1024
	ds_read_b128 v[176:179], v175 offset:2048
	ds_read_b128 v[180:183], v175 offset:3072
	s_add_u32 s54, s10, 0xfff80080
	s_addc_u32 s55, s11, -1
	s_cmp_eq_u32 s49, 28
	s_cselect_b32 s61, s9, s55
	s_cselect_b32 s60, s18, s54
	s_cselect_b32 s55, s19, s47
	s_cselect_b32 s54, s36, s37
	v_lshl_add_u64 v[200:201], s[10:11], 0, v[154:155]
	s_add_i32 m0, s57, 0xc000
	ds_read_b128 v[184:187], v174
	ds_read_b128 v[188:191], v174 offset:1024
	ds_read_b128 v[192:195], v174 offset:2048
	ds_read_b128 v[196:199], v174 offset:3072
	ds_read_b128 v[204:207], v174 offset:4096
	ds_read_b128 v[208:211], v174 offset:5120
	ds_read_b128 v[212:215], v174 offset:6144
	ds_read_b128 v[216:219], v174 offset:7168
	global_load_lds_dwordx4 v[200:201], off
	v_lshl_add_u64 v[200:201], s[10:11], 0, v[156:157]
	s_add_i32 m0, s57, 0xe000
	s_nop 0
	global_load_lds_dwordx4 v[200:201], off
	s_waitcnt vmcnt(8) lgkmcnt(0)
	s_setprio 1
	s_barrier
	v_mfma_f32_16x16x32_bf16 v[114:117], v[130:133], v[184:187], v[114:117]
	v_mfma_f32_16x16x32_bf16 v[118:121], v[138:141], v[184:187], v[118:121]
	v_mfma_f32_16x16x32_bf16 v[98:101], v[130:133], v[192:195], v[98:101]
	v_mfma_f32_16x16x32_bf16 v[102:105], v[138:141], v[192:195], v[102:105]
	v_mfma_f32_16x16x32_bf16 v[82:85], v[130:133], v[204:207], v[82:85]
	v_mfma_f32_16x16x32_bf16 v[86:89], v[138:141], v[204:207], v[86:89]
	v_mfma_f32_16x16x32_bf16 v[66:69], v[130:133], v[212:215], v[66:69]
	v_mfma_f32_16x16x32_bf16 v[70:73], v[138:141], v[212:215], v[70:73]
	v_mfma_f32_16x16x32_bf16 v[114:117], v[134:137], v[188:191], v[114:117]
	v_mfma_f32_16x16x32_bf16 v[118:121], v[142:145], v[188:191], v[118:121]
	v_mfma_f32_16x16x32_bf16 v[98:101], v[134:137], v[196:199], v[98:101]
	v_mfma_f32_16x16x32_bf16 v[102:105], v[142:145], v[196:199], v[102:105]
	v_mfma_f32_16x16x32_bf16 v[82:85], v[134:137], v[208:211], v[82:85]
	v_mfma_f32_16x16x32_bf16 v[86:89], v[142:145], v[208:211], v[86:89]
	v_mfma_f32_16x16x32_bf16 v[66:69], v[134:137], v[216:219], v[66:69]
	v_mfma_f32_16x16x32_bf16 v[70:73], v[142:145], v[216:219], v[70:73]
	v_mfma_f32_16x16x32_bf16 v[122:125], v[162:165], v[184:187], v[122:125]
	v_mfma_f32_16x16x32_bf16 v[126:129], v[176:179], v[184:187], v[126:129]
	v_mfma_f32_16x16x32_bf16 v[106:109], v[162:165], v[192:195], v[106:109]
	v_mfma_f32_16x16x32_bf16 v[110:113], v[176:179], v[192:195], v[110:113]
	v_mfma_f32_16x16x32_bf16 v[90:93], v[162:165], v[204:207], v[90:93]
	v_mfma_f32_16x16x32_bf16 v[94:97], v[176:179], v[204:207], v[94:97]
	v_mfma_f32_16x16x32_bf16 v[74:77], v[162:165], v[212:215], v[74:77]
	v_mfma_f32_16x16x32_bf16 v[78:81], v[176:179], v[212:215], v[78:81]
	v_mfma_f32_16x16x32_bf16 v[122:125], v[166:169], v[188:191], v[122:125]
	v_mfma_f32_16x16x32_bf16 v[126:129], v[180:183], v[188:191], v[126:129]
	v_mfma_f32_16x16x32_bf16 v[106:109], v[166:169], v[196:199], v[106:109]
	v_mfma_f32_16x16x32_bf16 v[110:113], v[180:183], v[196:199], v[110:113]
	v_mfma_f32_16x16x32_bf16 v[90:93], v[166:169], v[208:211], v[90:93]
	v_mfma_f32_16x16x32_bf16 v[94:97], v[180:183], v[208:211], v[94:97]
	v_mfma_f32_16x16x32_bf16 v[74:77], v[166:169], v[216:219], v[74:77]
	v_mfma_f32_16x16x32_bf16 v[78:81], v[180:183], v[216:219], v[78:81]
	s_barrier
	s_setprio 0
	s_add_i32 s59, s79, s66
	v_lshl_add_u64 v[200:201], s[54:55], 0, v[148:149]
	s_mov_b32 m0, s59
	ds_read_b128 v[184:187], v174 offset:16384
	ds_read_b128 v[188:191], v174 offset:17408
	ds_read_b128 v[192:195], v174 offset:18432
	ds_read_b128 v[196:199], v174 offset:19456
	ds_read_b128 v[204:207], v174 offset:20480
	ds_read_b128 v[208:211], v174 offset:21504
	ds_read_b128 v[212:215], v174 offset:22528
	ds_read_b128 v[216:219], v174 offset:23552
	global_load_lds_dwordx4 v[200:201], off
	s_add_i32 m0, s59, 0x2000
	s_add_u32 s62, s54, 0x80000
	v_lshl_add_u64 v[220:221], s[54:55], 0, v[152:153]
	s_addc_u32 s63, s55, 0
	s_add_i32 s59, s80, s66
	global_load_lds_dwordx4 v[220:221], off
	v_lshl_add_u64 v[222:223], s[62:63], 0, v[148:149]
	s_mov_b32 m0, s59
	v_lshl_add_u64 v[224:225], s[60:61], 0, v[150:151]
	global_load_lds_dwordx4 v[222:223], off
	v_lshl_add_u64 v[222:223], s[62:63], 0, v[152:153]
	s_add_i32 m0, s59, 0x2000
	s_nop 0
	global_load_lds_dwordx4 v[222:223], off
	v_lshl_add_u64 v[222:223], s[60:61], 0, v[146:147]
	s_mov_b32 m0, s57
	s_nop 0
	global_load_lds_dwordx4 v[222:223], off
	s_mov_b32 m0, s67
	s_nop 0
	global_load_lds_dwordx4 v[224:225], off
	s_waitcnt vmcnt(8) lgkmcnt(0)
	s_setprio 1
	s_barrier
; #define PG8_STAGE(bufoff, gbase, voff) do { _Pragma("unroll") for (int _i = 0; _i < 2; ++_i) \
;         __builtin_amdgcn_global_load_lds((const unsigned*)((const char*)(gbase) + (voff)[_i]), (PG8_LAS unsigned*)(lds + (bufoff) + ldsw + _i * 8192), 16, 0, 0); } while (0)
; #define PG8_LDA(dst, b, h) do { _Pragma("unroll") for (int m = 0; m < 4; ++m) _Pragma("unroll") for (int k = 0; k < 2; ++k) dst[m][k] = *(const PG8_LAS bf16x8*)(lds + PG8_SA(b, h) + aoff + m * 2048 + k * 1024); } while (0)
; #define PG8_LDB(dst, b, h) do { _Pragma("unroll") for (int n = 0; n < 2; ++n) _Pragma("unroll") for (int k = 0; k < 2; ++k) dst[n][k] = *(const PG8_LAS bf16x8*)(lds + PG8_SB(b, h) + boff + n * 2048 + k * 1024); } while (0)
; #define PG8_MMA(ai, bj, At, Bt) do { __builtin_amdgcn_s_setprio(1); _Pragma("unroll") for (int m = 0; m < 4; ++m) _Pragma("unroll") for (int n = 0; n < 2; ++n) _Pragma("unroll") for (int k = 0; k < 2; ++k) \
;         acc[ai][bj][m][n] = __builtin_amdgcn_mfma_f32_16x16x32_bf16(Bt[n][k], At[m][k], acc[ai][bj][m][n], 0, 0, 0); __builtin_amdgcn_s_setprio(0); } while (0)
; #define PG8_WAIT_V(n) asm volatile("s_waitcnt vmcnt(" #n ")" ::: "memory")
; #define PG8_WAIT_L(n) asm volatile("s_waitcnt lgkmcnt(" #n ")" ::: "memory")
; #define PG8_BAR __builtin_amdgcn_s_barrier()
; #define PG8_SCHED __builtin_amdgcn_sched_barrier(0)
; template <class Epi, class Sched, bool ALIGN_EPI = false, bool SP2 = false>
; __device__ __forceinline__ void gemm_phase(PG8_LAS unsigned char* lds, const Gemm g, const Sched& S, const Epi& E) {
;     ...
;             PG8_WAIT_V(8); PG8_WAIT_L(0); PG8_BAR; PG8_MMA(0, 0, At, B0); PG8_MMA(0, 1, At, B1); PG8_BAR; PG8_SCHED;
;             PG8_LDA(At, 0, 1); PG8_STAGE(PG8_SB(0, 0), b2, voffB); PG8_STAGE(PG8_SB(0, 1), b2 + hstep, voffB); PG8_STAGEA(PG8_SA(0, 0), a2, 0, last);
;             PG8_WAIT_V(8); PG8_WAIT_L(0); PG8_BAR; PG8_MMA(1, 0, At, B0); PG8_MMA(1, 1, At, B1); PG8_BAR; PG8_SCHED;
;             PG8_LDB(B0, 1, 0); PG8_LDB(B1, 1, 1); PG8_SCHED; PG8_LDA(At, 1, 0); PG8_STAGEA(PG8_SA(0, 1), a2, 1, last);
;             PG8_WAIT_V(8); PG8_WAIT_L(0); PG8_BAR; PG8_MMA(0, 0, At, B0); PG8_MMA(0, 1, At, B1); PG8_BAR; PG8_SCHED;
	v_mfma_f32_16x16x32_bf16 v[58:61], v[130:133], v[184:187], v[58:61]
	v_mfma_f32_16x16x32_bf16 v[62:65], v[138:141], v[184:187], v[62:65]
	v_mfma_f32_16x16x32_bf16 v[42:45], v[130:133], v[192:195], v[42:45]
	v_mfma_f32_16x16x32_bf16 v[46:49], v[138:141], v[192:195], v[46:49]
	v_mfma_f32_16x16x32_bf16 v[18:21], v[130:133], v[204:207], v[18:21]
	v_mfma_f32_16x16x32_bf16 v[22:25], v[138:141], v[204:207], v[22:25]
	v_mfma_f32_16x16x32_bf16 v[6:9], v[130:133], v[212:215], v[6:9]
	v_mfma_f32_16x16x32_bf16 v[14:17], v[138:141], v[212:215], v[14:17]
	v_mfma_f32_16x16x32_bf16 v[58:61], v[134:137], v[188:191], v[58:61]
	v_mfma_f32_16x16x32_bf16 v[62:65], v[142:145], v[188:191], v[62:65]
	v_mfma_f32_16x16x32_bf16 v[42:45], v[134:137], v[196:199], v[42:45]
	v_mfma_f32_16x16x32_bf16 v[46:49], v[142:145], v[196:199], v[46:49]
	v_mfma_f32_16x16x32_bf16 v[18:21], v[134:137], v[208:211], v[18:21]
	v_mfma_f32_16x16x32_bf16 v[22:25], v[142:145], v[208:211], v[22:25]
	v_mfma_f32_16x16x32_bf16 v[6:9], v[134:137], v[216:219], v[6:9]
	v_mfma_f32_16x16x32_bf16 v[14:17], v[142:145], v[216:219], v[14:17]
	v_mfma_f32_16x16x32_bf16 v[50:53], v[162:165], v[184:187], v[50:53]
	v_mfma_f32_16x16x32_bf16 v[54:57], v[176:179], v[184:187], v[54:57]
	v_mfma_f32_16x16x32_bf16 v[34:37], v[162:165], v[192:195], v[34:37]
	v_mfma_f32_16x16x32_bf16 v[38:41], v[176:179], v[192:195], v[38:41]
	v_mfma_f32_16x16x32_bf16 v[26:29], v[162:165], v[204:207], v[26:29]
	v_mfma_f32_16x16x32_bf16 v[30:33], v[176:179], v[204:207], v[30:33]
	v_mfma_f32_16x16x32_bf16 v[10:13], v[162:165], v[212:215], v[10:13]
	v_mfma_f32_16x16x32_bf16 v[2:5], v[176:179], v[212:215], v[2:5]
	v_mfma_f32_16x16x32_bf16 v[50:53], v[166:169], v[188:191], v[50:53]
	v_mfma_f32_16x16x32_bf16 v[54:57], v[180:183], v[188:191], v[54:57]
	v_mfma_f32_16x16x32_bf16 v[34:37], v[166:169], v[196:199], v[34:37]
	v_mfma_f32_16x16x32_bf16 v[38:41], v[180:183], v[196:199], v[38:41]
	v_mfma_f32_16x16x32_bf16 v[26:29], v[166:169], v[208:211], v[26:29]
	v_mfma_f32_16x16x32_bf16 v[30:33], v[180:183], v[208:211], v[30:33]
	v_mfma_f32_16x16x32_bf16 v[10:13], v[166:169], v[216:219], v[10:13]
	v_mfma_f32_16x16x32_bf16 v[2:5], v[180:183], v[216:219], v[2:5]
	s_barrier
	s_setprio 0
	s_add_i32 s59, 0, 0x18000
	s_add_i32 s62, 0, 0x1c000
	v_add_u32_e32 v142, s59, v170
	v_add_u32_e32 v175, s62, v170
	ds_read_b128 v[130:133], v142
	ds_read_b128 v[134:137], v142 offset:1024
	ds_read_b128 v[138:141], v142 offset:2048
	ds_read_b128 v[142:145], v142 offset:3072
	ds_read_b128 v[162:165], v175
	ds_read_b128 v[166:169], v175 offset:1024
	ds_read_b128 v[176:179], v175 offset:2048
	ds_read_b128 v[180:183], v175 offset:3072
	s_add_u32 s60, s60, 0x80000
	s_addc_u32 s61, s61, 0
	s_mov_b32 m0, s68
	v_lshl_add_u64 v[226:227], s[60:61], 0, v[146:147]
	ds_read_b128 v[184:187], v174 offset:32768
	ds_read_b128 v[188:191], v174 offset:33792
	ds_read_b128 v[192:195], v174 offset:34816
	ds_read_b128 v[196:199], v174 offset:35840
	ds_read_b128 v[204:207], v174 offset:36864
	ds_read_b128 v[208:211], v174 offset:37888
	ds_read_b128 v[212:215], v174 offset:38912
	ds_read_b128 v[216:219], v174 offset:39936
	global_load_lds_dwordx4 v[226:227], off
	v_lshl_add_u64 v[226:227], s[60:61], 0, v[150:151]
	s_mov_b32 m0, s69
	s_nop 0
	global_load_lds_dwordx4 v[226:227], off
	s_waitcnt vmcnt(8) lgkmcnt(0)
	s_setprio 1
	s_barrier
	v_mfma_f32_16x16x32_bf16 v[114:117], v[130:133], v[184:187], v[114:117]
	v_mfma_f32_16x16x32_bf16 v[118:121], v[138:141], v[184:187], v[118:121]
	v_mfma_f32_16x16x32_bf16 v[98:101], v[130:133], v[192:195], v[98:101]
	v_mfma_f32_16x16x32_bf16 v[102:105], v[138:141], v[192:195], v[102:105]
	v_mfma_f32_16x16x32_bf16 v[82:85], v[130:133], v[204:207], v[82:85]
	v_mfma_f32_16x16x32_bf16 v[86:89], v[138:141], v[204:207], v[86:89]
	v_mfma_f32_16x16x32_bf16 v[66:69], v[130:133], v[212:215], v[66:69]
	v_mfma_f32_16x16x32_bf16 v[70:73], v[138:141], v[212:215], v[70:73]
	v_mfma_f32_16x16x32_bf16 v[114:117], v[134:137], v[188:191], v[114:117]
	v_mfma_f32_16x16x32_bf16 v[118:121], v[142:145], v[188:191], v[118:121]
	v_mfma_f32_16x16x32_bf16 v[98:101], v[134:137], v[196:199], v[98:101]
	v_mfma_f32_16x16x32_bf16 v[102:105], v[142:145], v[196:199], v[102:105]
	v_mfma_f32_16x16x32_bf16 v[82:85], v[134:137], v[208:211], v[82:85]
	v_mfma_f32_16x16x32_bf16 v[86:89], v[142:145], v[208:211], v[86:89]
	v_mfma_f32_16x16x32_bf16 v[66:69], v[134:137], v[216:219], v[66:69]
	v_mfma_f32_16x16x32_bf16 v[70:73], v[142:145], v[216:219], v[70:73]
	v_mfma_f32_16x16x32_bf16 v[122:125], v[162:165], v[184:187], v[122:125]
	v_mfma_f32_16x16x32_bf16 v[126:129], v[176:179], v[184:187], v[126:129]
	v_mfma_f32_16x16x32_bf16 v[106:109], v[162:165], v[192:195], v[106:109]
	v_mfma_f32_16x16x32_bf16 v[110:113], v[176:179], v[192:195], v[110:113]
	v_mfma_f32_16x16x32_bf16 v[90:93], v[162:165], v[204:207], v[90:93]
	v_mfma_f32_16x16x32_bf16 v[94:97], v[176:179], v[204:207], v[94:97]
	v_mfma_f32_16x16x32_bf16 v[74:77], v[162:165], v[212:215], v[74:77]
	v_mfma_f32_16x16x32_bf16 v[78:81], v[176:179], v[212:215], v[78:81]
	v_mfma_f32_16x16x32_bf16 v[122:125], v[166:169], v[188:191], v[122:125]
	v_mfma_f32_16x16x32_bf16 v[126:129], v[180:183], v[188:191], v[126:129]
	v_mfma_f32_16x16x32_bf16 v[106:109], v[166:169], v[196:199], v[106:109]
	v_mfma_f32_16x16x32_bf16 v[110:113], v[180:183], v[196:199], v[110:113]
	v_mfma_f32_16x16x32_bf16 v[90:93], v[166:169], v[208:211], v[90:93]
	v_mfma_f32_16x16x32_bf16 v[94:97], v[180:183], v[208:211], v[94:97]
	v_mfma_f32_16x16x32_bf16 v[74:77], v[166:169], v[216:219], v[74:77]
	v_mfma_f32_16x16x32_bf16 v[78:81], v[180:183], v[216:219], v[78:81]
	s_barrier
; #define PG8_STAGE(bufoff, gbase, voff) do { _Pragma("unroll") for (int _i = 0; _i < 2; ++_i) \
;         __builtin_amdgcn_global_load_lds((const unsigned*)((const char*)(gbase) + (voff)[_i]), (PG8_LAS unsigned*)(lds + (bufoff) + ldsw + _i * 8192), 16, 0, 0); } while (0)
; #define PG8_LDA(dst, b, h) do { _Pragma("unroll") for (int m = 0; m < 4; ++m) _Pragma("unroll") for (int k = 0; k < 2; ++k) dst[m][k] = *(const PG8_LAS bf16x8*)(lds + PG8_SA(b, h) + aoff + m * 2048 + k * 1024); } while (0)
; #define PG8_MMA(ai, bj, At, Bt) do { __builtin_amdgcn_s_setprio(1); _Pragma("unroll") for (int m = 0; m < 4; ++m) _Pragma("unroll") for (int n = 0; n < 2; ++n) _Pragma("unroll") for (int k = 0; k < 2; ++k) \
;         acc[ai][bj][m][n] = __builtin_amdgcn_mfma_f32_16x16x32_bf16(Bt[n][k], At[m][k], acc[ai][bj][m][n], 0, 0, 0); __builtin_amdgcn_s_setprio(0); } while (0)
; #define PG8_WAIT_V(n) asm volatile("s_waitcnt vmcnt(" #n ")" ::: "memory")
; #define PG8_WAIT_L(n) asm volatile("s_waitcnt lgkmcnt(" #n ")" ::: "memory")
; #define PG8_BAR __builtin_amdgcn_s_barrier()
; #define PG8_SCHED __builtin_amdgcn_sched_barrier(0)
; template <class Epi, class Sched, bool ALIGN_EPI = false, bool SP2 = false>
; __device__ __forceinline__ void gemm_phase(PG8_LAS unsigned char* lds, const Gemm g, const Sched& S, const Epi& E) {
;     ...
;             PG8_LDA(At, 1, 1); PG8_STAGE(PG8_SB(1, 0), b3, voffB); PG8_STAGE(PG8_SB(1, 1), b3 + hstep, voffB); PG8_STAGEA(PG8_SA(1, 0), a3, 0, last);
;             PG8_WAIT_V(8); PG8_WAIT_L(0); PG8_BAR; PG8_MMA(1, 0, At, B0); PG8_MMA(1, 1, At, B1); PG8_BAR; PG8_SCHED;
;     ...
;         if constexpr (ALIGN_EPI) { if (wr == 0) PG8_BAR; }
	s_setprio 0
	s_add_i32 s59, s59, s66
	v_lshl_add_u64 v[200:201], v[200:201], 0, s[26:27]
	s_mov_b32 m0, s59
	ds_read_b128 v[184:187], v174 offset:49152
	ds_read_b128 v[188:191], v174 offset:50176
	ds_read_b128 v[192:195], v174 offset:51200
	ds_read_b128 v[196:199], v174 offset:52224
	ds_read_b128 v[204:207], v174 offset:53248
	ds_read_b128 v[208:211], v174 offset:54272
	ds_read_b128 v[212:215], v174 offset:55296
	ds_read_b128 v[216:219], v174 offset:56320
	global_load_lds_dwordx4 v[200:201], off
	s_add_i32 m0, s59, 0x2000
	s_add_u32 s54, s54, 0x80080
	v_lshl_add_u64 v[200:201], v[220:221], 0, s[26:27]
	s_addc_u32 s55, s55, 0
	s_add_i32 s59, s62, s66
	global_load_lds_dwordx4 v[200:201], off
	v_lshl_add_u64 v[200:201], s[54:55], 0, v[148:149]
	s_mov_b32 m0, s59
	s_nop 0
	global_load_lds_dwordx4 v[200:201], off
	v_lshl_add_u64 v[200:201], s[54:55], 0, v[152:153]
	s_add_i32 m0, s59, 0x2000
	s_nop 0
	global_load_lds_dwordx4 v[200:201], off
	v_lshl_add_u64 v[200:201], v[222:223], 0, s[26:27]
	s_mov_b32 m0, s74
	s_nop 0
	global_load_lds_dwordx4 v[200:201], off
	v_lshl_add_u64 v[200:201], v[224:225], 0, s[26:27]
	s_mov_b32 m0, s75
	s_nop 0
	global_load_lds_dwordx4 v[200:201], off
	s_waitcnt vmcnt(8) lgkmcnt(0)
	s_setprio 1
	s_barrier
	v_mfma_f32_16x16x32_bf16 v[58:61], v[130:133], v[184:187], v[58:61]
	v_mfma_f32_16x16x32_bf16 v[62:65], v[138:141], v[184:187], v[62:65]
	v_mfma_f32_16x16x32_bf16 v[42:45], v[130:133], v[192:195], v[42:45]
	v_mfma_f32_16x16x32_bf16 v[46:49], v[138:141], v[192:195], v[46:49]
	v_mfma_f32_16x16x32_bf16 v[18:21], v[130:133], v[204:207], v[18:21]
	v_mfma_f32_16x16x32_bf16 v[22:25], v[138:141], v[204:207], v[22:25]
	v_mfma_f32_16x16x32_bf16 v[6:9], v[130:133], v[212:215], v[6:9]
	v_mfma_f32_16x16x32_bf16 v[14:17], v[138:141], v[212:215], v[14:17]
	v_mfma_f32_16x16x32_bf16 v[58:61], v[134:137], v[188:191], v[58:61]
	v_mfma_f32_16x16x32_bf16 v[62:65], v[142:145], v[188:191], v[62:65]
	v_mfma_f32_16x16x32_bf16 v[42:45], v[134:137], v[196:199], v[42:45]
	v_mfma_f32_16x16x32_bf16 v[46:49], v[142:145], v[196:199], v[46:49]
	v_mfma_f32_16x16x32_bf16 v[18:21], v[134:137], v[208:211], v[18:21]
	v_mfma_f32_16x16x32_bf16 v[22:25], v[142:145], v[208:211], v[22:25]
	v_mfma_f32_16x16x32_bf16 v[6:9], v[134:137], v[216:219], v[6:9]
	v_mfma_f32_16x16x32_bf16 v[14:17], v[142:145], v[216:219], v[14:17]
	v_mfma_f32_16x16x32_bf16 v[50:53], v[162:165], v[184:187], v[50:53]
	v_mfma_f32_16x16x32_bf16 v[54:57], v[176:179], v[184:187], v[54:57]
	v_mfma_f32_16x16x32_bf16 v[34:37], v[162:165], v[192:195], v[34:37]
	v_mfma_f32_16x16x32_bf16 v[38:41], v[176:179], v[192:195], v[38:41]
	v_mfma_f32_16x16x32_bf16 v[26:29], v[162:165], v[204:207], v[26:29]
	v_mfma_f32_16x16x32_bf16 v[30:33], v[176:179], v[204:207], v[30:33]
	v_mfma_f32_16x16x32_bf16 v[10:13], v[162:165], v[212:215], v[10:13]
	v_mfma_f32_16x16x32_bf16 v[2:5], v[176:179], v[212:215], v[2:5]
	v_mfma_f32_16x16x32_bf16 v[50:53], v[166:169], v[188:191], v[50:53]
	v_mfma_f32_16x16x32_bf16 v[54:57], v[180:183], v[188:191], v[54:57]
	v_mfma_f32_16x16x32_bf16 v[34:37], v[166:169], v[196:199], v[34:37]
	v_mfma_f32_16x16x32_bf16 v[38:41], v[180:183], v[196:199], v[38:41]
	v_mfma_f32_16x16x32_bf16 v[26:29], v[166:169], v[208:211], v[26:29]
	v_mfma_f32_16x16x32_bf16 v[30:33], v[180:183], v[208:211], v[30:33]
	v_mfma_f32_16x16x32_bf16 v[10:13], v[166:169], v[216:219], v[10:13]
	v_mfma_f32_16x16x32_bf16 v[2:5], v[180:183], v[216:219], v[2:5]
	s_barrier
	s_setprio 0
	s_add_i32 s49, s49, 2
	s_add_u32 s10, s10, 0x100
	s_addc_u32 s11, s11, 0
	s_add_u32 s37, s37, 0x100
	s_addc_u32 s47, s47, 0
	s_cmp_gt_u32 s49, 29
	s_cbranch_scc0 .LBB0_110
	s_and_b64 vcc, exec, s[38:39]
	s_cbranch_vccz .LBB0_113
	s_barrier

; #define PG8_STAGE(bufoff, gbase, voff) do { _Pragma("unroll") for (int _i = 0; _i < 2; ++_i) \
;         __builtin_amdgcn_global_load_lds((const unsigned*)((const char*)(gbase) + (voff)[_i]), (PG8_LAS unsigned*)(lds + (bufoff) + ldsw + _i * 8192), 16, 0, 0); } while (0)
; #define PG8_LDA(dst, b, h) do { _Pragma("unroll") for (int m = 0; m < 4; ++m) _Pragma("unroll") for (int k = 0; k < 2; ++k) dst[m][k] = *(const PG8_LAS bf16x8*)(lds + PG8_SA(b, h) + aoff + m * 2048 + k * 1024); } while (0)
; #define PG8_LDB(dst, b, h) do { _Pragma("unroll") for (int n = 0; n < 2; ++n) _Pragma("unroll") for (int k = 0; k < 2; ++k) dst[n][k] = *(const PG8_LAS bf16x8*)(lds + PG8_SB(b, h) + boff + n * 2048 + k * 1024); } while (0)
; #define PG8_MMA(ai, bj, At, Bt) do { __builtin_amdgcn_s_setprio(1); _Pragma("unroll") for (int m = 0; m < 4; ++m) _Pragma("unroll") for (int n = 0; n < 2; ++n) _Pragma("unroll") for (int k = 0; k < 2; ++k) \
;         acc[ai][bj][m][n] = __builtin_amdgcn_mfma_f32_16x16x32_bf16(Bt[n][k], At[m][k], acc[ai][bj][m][n], 0, 0, 0); __builtin_amdgcn_s_setprio(0); } while (0)
; #define PG8_WAIT_V(n) asm volatile("s_waitcnt vmcnt(" #n ")" ::: "memory")
; #define PG8_WAIT_L(n) asm volatile("s_waitcnt lgkmcnt(" #n ")" ::: "memory")
; template <class Epi, class Sched, bool ALIGN_EPI = false, bool SP2 = false>
; __device__ __forceinline__ void gemm_phase(PG8_LAS unsigned char* lds, const Gemm g, const Sched& S, const Epi& E) {
;     ...
;             const bool last = (t == nt - 2);
;             const char* a1 = cA + (size_t)(t + 1) * kstep;
;             const char* a2 = last ? nA : cA + (size_t)(t + 2) * kstep; const char* b2 = last ? nB : cB + (size_t)(t + 2) * kstep;
;             const char* a3 = a2 + kstep; const char* b3 = b2 + kstep;
;             if (last && has_next) S.a_ready(nxt);
;             if constexpr (SP2) {
;             PG8_LDB(B0, 0, 0); PG8_LDB(B1, 0, 1); PG8_SCHED; PG8_LDA(At, 0, 0); PG8_STAGEA(PG8_SA(1, 1), a1, 1, false);
;             PG8_WAIT_V(8); PG8_WAIT_L(0); PG8_BAR; PG8_MMA(0, 0, At, B0); PG8_MMA(0, 1, At, B1); PG8_BAR; PG8_SCHED;
;             PG8_LDA(At, 0, 1); PG8_STAGE(PG8_SB(0, 0), b2, voffB); PG8_STAGE(PG8_SB(0, 1), b2 + hstep, voffB); PG8_STAGEA(PG8_SA(0, 0), a2, 0, last);
;             PG8_WAIT_V(8); PG8_WAIT_L(0); PG8_BAR; PG8_MMA(1, 0, At, B0); PG8_MMA(1, 1, At, B1); PG8_BAR; PG8_SCHED;
.LBB0_383:
	v_add_u32_e32 v142, s79, v173
	v_add_u32_e32 v170, s80, v173
	ds_read_b128 v[130:133], v142
	ds_read_b128 v[134:137], v142 offset:1024
	ds_read_b128 v[138:141], v142 offset:2048
	ds_read_b128 v[142:145], v142 offset:3072
	ds_read_b128 v[146:149], v170
	ds_read_b128 v[150:153], v170 offset:1024
	ds_read_b128 v[154:157], v170 offset:2048
	ds_read_b128 v[176:179], v170 offset:3072
	s_add_i32 s58, s56, 1
	s_ashr_i32 s59, s58, 31
	s_mov_b32 s62, s56
	s_add_i32 s56, s56, 2
	s_lshl_b64 s[96:97], s[58:59], 7
	s_cmp_eq_u32 s62, 30
	s_cselect_b32 s63, s9, s36
	s_cselect_b32 s62, s49, s19
	s_cselect_b32 s59, s89, s57
	s_cselect_b32 s58, s90, s37
	s_add_u32 s95, s10, s96
	s_addc_u32 s97, s11, s97
	s_add_u32 s96, s95, 0x80000
	s_addc_u32 s97, s97, 0
	v_lshl_add_u64 v[170:171], s[96:97], 0, v[158:159]
	s_add_i32 m0, s66, 0xc000
	ds_read_b128 v[180:183], v174
	ds_read_b128 v[184:187], v174 offset:1024
	ds_read_b128 v[188:191], v174 offset:2048
	ds_read_b128 v[192:195], v174 offset:3072
	ds_read_b128 v[196:199], v174 offset:4096
	ds_read_b128 v[204:207], v174 offset:5120
	ds_read_b128 v[208:211], v174 offset:6144
	ds_read_b128 v[212:215], v174 offset:7168
	global_load_lds_dwordx4 v[170:171], off
	v_lshl_add_u64 v[170:171], s[96:97], 0, v[162:163]
	s_add_i32 m0, s66, 0xe000
	s_nop 0
	global_load_lds_dwordx4 v[170:171], off
	s_waitcnt vmcnt(8) lgkmcnt(0)
	s_setprio 1
	s_barrier
	v_mfma_f32_16x16x32_bf16 v[118:121], v[130:133], v[180:183], v[118:121]
	v_mfma_f32_16x16x32_bf16 v[114:117], v[138:141], v[180:183], v[114:117]
	v_mfma_f32_16x16x32_bf16 v[102:105], v[130:133], v[188:191], v[102:105]
	v_mfma_f32_16x16x32_bf16 v[98:101], v[138:141], v[188:191], v[98:101]
	v_mfma_f32_16x16x32_bf16 v[86:89], v[130:133], v[196:199], v[86:89]
	v_mfma_f32_16x16x32_bf16 v[82:85], v[138:141], v[196:199], v[82:85]
	v_mfma_f32_16x16x32_bf16 v[70:73], v[130:133], v[208:211], v[70:73]
	v_mfma_f32_16x16x32_bf16 v[66:69], v[138:141], v[208:211], v[66:69]
	v_mfma_f32_16x16x32_bf16 v[118:121], v[134:137], v[184:187], v[118:121]
	v_mfma_f32_16x16x32_bf16 v[114:117], v[142:145], v[184:187], v[114:117]
	v_mfma_f32_16x16x32_bf16 v[102:105], v[134:137], v[192:195], v[102:105]
	v_mfma_f32_16x16x32_bf16 v[98:101], v[142:145], v[192:195], v[98:101]
	v_mfma_f32_16x16x32_bf16 v[86:89], v[134:137], v[204:207], v[86:89]
	v_mfma_f32_16x16x32_bf16 v[82:85], v[142:145], v[204:207], v[82:85]
	v_mfma_f32_16x16x32_bf16 v[70:73], v[134:137], v[212:215], v[70:73]
	v_mfma_f32_16x16x32_bf16 v[66:69], v[142:145], v[212:215], v[66:69]
	v_mfma_f32_16x16x32_bf16 v[126:129], v[146:149], v[180:183], v[126:129]
	v_mfma_f32_16x16x32_bf16 v[122:125], v[154:157], v[180:183], v[122:125]
	v_mfma_f32_16x16x32_bf16 v[110:113], v[146:149], v[188:191], v[110:113]
	v_mfma_f32_16x16x32_bf16 v[106:109], v[154:157], v[188:191], v[106:109]
	v_mfma_f32_16x16x32_bf16 v[94:97], v[146:149], v[196:199], v[94:97]
	v_mfma_f32_16x16x32_bf16 v[90:93], v[154:157], v[196:199], v[90:93]
	v_mfma_f32_16x16x32_bf16 v[78:81], v[146:149], v[208:211], v[78:81]
	v_mfma_f32_16x16x32_bf16 v[74:77], v[154:157], v[208:211], v[74:77]
	v_mfma_f32_16x16x32_bf16 v[126:129], v[150:153], v[184:187], v[126:129]
	v_mfma_f32_16x16x32_bf16 v[122:125], v[176:179], v[184:187], v[122:125]
	v_mfma_f32_16x16x32_bf16 v[110:113], v[150:153], v[192:195], v[110:113]
	v_mfma_f32_16x16x32_bf16 v[106:109], v[176:179], v[192:195], v[106:109]
	v_mfma_f32_16x16x32_bf16 v[94:97], v[150:153], v[204:207], v[94:97]
	v_mfma_f32_16x16x32_bf16 v[90:93], v[176:179], v[204:207], v[90:93]
	v_mfma_f32_16x16x32_bf16 v[78:81], v[150:153], v[212:215], v[78:81]
	v_mfma_f32_16x16x32_bf16 v[74:77], v[176:179], v[212:215], v[74:77]
	s_barrier
	s_setprio 0
	s_add_i32 s95, s79, s65
	v_lshl_add_u64 v[170:171], s[58:59], 0, v[160:161]
	s_mov_b32 m0, s95
	ds_read_b128 v[180:183], v174 offset:16384
	ds_read_b128 v[184:187], v174 offset:17408
	ds_read_b128 v[188:191], v174 offset:18432
	ds_read_b128 v[192:195], v174 offset:19456
	ds_read_b128 v[196:199], v174 offset:20480
	ds_read_b128 v[204:207], v174 offset:21504
	ds_read_b128 v[208:211], v174 offset:22528
	ds_read_b128 v[212:215], v174 offset:23552
	global_load_lds_dwordx4 v[170:171], off
	s_add_i32 m0, s95, 0x2000
	s_add_u32 s96, s58, 0x80000
	v_lshl_add_u64 v[200:201], s[58:59], 0, v[164:165]
	s_addc_u32 s97, s59, 0
	s_add_i32 s95, s80, s65
	global_load_lds_dwordx4 v[200:201], off
	v_lshl_add_u64 v[216:217], s[96:97], 0, v[160:161]
	s_mov_b32 m0, s95
	v_lshl_add_u64 v[218:219], s[62:63], 0, v[162:163]
	global_load_lds_dwordx4 v[216:217], off
	v_lshl_add_u64 v[216:217], s[96:97], 0, v[164:165]
	s_add_i32 m0, s95, 0x2000
	s_nop 0
	global_load_lds_dwordx4 v[216:217], off
	v_lshl_add_u64 v[216:217], s[62:63], 0, v[158:159]
	s_mov_b32 m0, s66
	s_nop 0
	global_load_lds_dwordx4 v[216:217], off
	s_mov_b32 m0, s67
	s_nop 0
	global_load_lds_dwordx4 v[218:219], off
	s_waitcnt vmcnt(8) lgkmcnt(0)
	s_setprio 1
	s_barrier
; #define PG8_LDA(dst, b, h) do { _Pragma("unroll") for (int m = 0; m < 4; ++m) _Pragma("unroll") for (int k = 0; k < 2; ++k) dst[m][k] = *(const PG8_LAS bf16x8*)(lds + PG8_SA(b, h) + aoff + m * 2048 + k * 1024); } while (0)
; #define PG8_LDB(dst, b, h) do { _Pragma("unroll") for (int n = 0; n < 2; ++n) _Pragma("unroll") for (int k = 0; k < 2; ++k) dst[n][k] = *(const PG8_LAS bf16x8*)(lds + PG8_SB(b, h) + boff + n * 2048 + k * 1024); } while (0)
; #define PG8_MMA(ai, bj, At, Bt) do { __builtin_amdgcn_s_setprio(1); _Pragma("unroll") for (int m = 0; m < 4; ++m) _Pragma("unroll") for (int n = 0; n < 2; ++n) _Pragma("unroll") for (int k = 0; k < 2; ++k) \
;         acc[ai][bj][m][n] = __builtin_amdgcn_mfma_f32_16x16x32_bf16(Bt[n][k], At[m][k], acc[ai][bj][m][n], 0, 0, 0); __builtin_amdgcn_s_setprio(0); } while (0)
; #define PG8_WAIT_V(n) asm volatile("s_waitcnt vmcnt(" #n ")" ::: "memory")
; #define PG8_WAIT_L(n) asm volatile("s_waitcnt lgkmcnt(" #n ")" ::: "memory")
; #define PG8_BAR __builtin_amdgcn_s_barrier()
; #define PG8_SCHED __builtin_amdgcn_sched_barrier(0)
; template <class Epi, class Sched, bool ALIGN_EPI = false, bool SP2 = false>
; __device__ __forceinline__ void gemm_phase(PG8_LAS unsigned char* lds, const Gemm g, const Sched& S, const Epi& E) {
;     ...
;             PG8_WAIT_V(8); PG8_WAIT_L(0); PG8_BAR; PG8_MMA(1, 0, At, B0); PG8_MMA(1, 1, At, B1); PG8_BAR; PG8_SCHED;
;             PG8_LDB(B0, 1, 0); PG8_LDB(B1, 1, 1); PG8_SCHED; PG8_LDA(At, 1, 0); PG8_STAGEA(PG8_SA(0, 1), a2, 1, last);
;             PG8_WAIT_V(8); PG8_WAIT_L(0); PG8_BAR; PG8_MMA(0, 0, At, B0); PG8_MMA(0, 1, At, B1); PG8_BAR; PG8_SCHED;
	v_mfma_f32_16x16x32_bf16 v[54:57], v[130:133], v[180:183], v[54:57]
	v_mfma_f32_16x16x32_bf16 v[50:53], v[138:141], v[180:183], v[50:53]
	v_mfma_f32_16x16x32_bf16 v[38:41], v[130:133], v[188:191], v[38:41]
	v_mfma_f32_16x16x32_bf16 v[34:37], v[138:141], v[188:191], v[34:37]
	v_mfma_f32_16x16x32_bf16 v[22:25], v[130:133], v[196:199], v[22:25]
	v_mfma_f32_16x16x32_bf16 v[18:21], v[138:141], v[196:199], v[18:21]
	v_mfma_f32_16x16x32_bf16 v[10:13], v[130:133], v[208:211], v[10:13]
	v_mfma_f32_16x16x32_bf16 v[6:9], v[138:141], v[208:211], v[6:9]
	v_mfma_f32_16x16x32_bf16 v[54:57], v[134:137], v[184:187], v[54:57]
	v_mfma_f32_16x16x32_bf16 v[50:53], v[142:145], v[184:187], v[50:53]
	v_mfma_f32_16x16x32_bf16 v[38:41], v[134:137], v[192:195], v[38:41]
	v_mfma_f32_16x16x32_bf16 v[34:37], v[142:145], v[192:195], v[34:37]
	v_mfma_f32_16x16x32_bf16 v[22:25], v[134:137], v[204:207], v[22:25]
	v_mfma_f32_16x16x32_bf16 v[18:21], v[142:145], v[204:207], v[18:21]
	v_mfma_f32_16x16x32_bf16 v[10:13], v[134:137], v[212:215], v[10:13]
	v_mfma_f32_16x16x32_bf16 v[6:9], v[142:145], v[212:215], v[6:9]
	v_mfma_f32_16x16x32_bf16 v[62:65], v[146:149], v[180:183], v[62:65]
	v_mfma_f32_16x16x32_bf16 v[58:61], v[154:157], v[180:183], v[58:61]
	v_mfma_f32_16x16x32_bf16 v[46:49], v[146:149], v[188:191], v[46:49]
	v_mfma_f32_16x16x32_bf16 v[42:45], v[154:157], v[188:191], v[42:45]
	v_mfma_f32_16x16x32_bf16 v[30:33], v[146:149], v[196:199], v[30:33]
	v_mfma_f32_16x16x32_bf16 v[26:29], v[154:157], v[196:199], v[26:29]
	v_mfma_f32_16x16x32_bf16 v[14:17], v[146:149], v[208:211], v[14:17]
	v_mfma_f32_16x16x32_bf16 v[2:5], v[154:157], v[208:211], v[2:5]
	v_mfma_f32_16x16x32_bf16 v[62:65], v[150:153], v[184:187], v[62:65]
	v_mfma_f32_16x16x32_bf16 v[58:61], v[176:179], v[184:187], v[58:61]
	v_mfma_f32_16x16x32_bf16 v[46:49], v[150:153], v[192:195], v[46:49]
	v_mfma_f32_16x16x32_bf16 v[42:45], v[176:179], v[192:195], v[42:45]
	v_mfma_f32_16x16x32_bf16 v[30:33], v[150:153], v[204:207], v[30:33]
	v_mfma_f32_16x16x32_bf16 v[26:29], v[176:179], v[204:207], v[26:29]
	v_mfma_f32_16x16x32_bf16 v[14:17], v[150:153], v[212:215], v[14:17]
	v_mfma_f32_16x16x32_bf16 v[2:5], v[176:179], v[212:215], v[2:5]
	s_barrier
	s_setprio 0
	s_add_i32 s95, 0, 0x18000
	s_add_i32 s96, 0, 0x1c000
	v_add_u32_e32 v142, s95, v173
	v_add_u32_e32 v175, s96, v173
	ds_read_b128 v[130:133], v142
	ds_read_b128 v[134:137], v142 offset:1024
	ds_read_b128 v[138:141], v142 offset:2048
	ds_read_b128 v[142:145], v142 offset:3072
	ds_read_b128 v[146:149], v175
	ds_read_b128 v[150:153], v175 offset:1024
	ds_read_b128 v[154:157], v175 offset:2048
	ds_read_b128 v[176:179], v175 offset:3072
	s_add_u32 s62, s62, 0x80000
	s_addc_u32 s63, s63, 0
	s_mov_b32 m0, s68
	v_lshl_add_u64 v[220:221], s[62:63], 0, v[158:159]
	ds_read_b128 v[180:183], v174 offset:32768
	ds_read_b128 v[184:187], v174 offset:33792
	ds_read_b128 v[188:191], v174 offset:34816
	ds_read_b128 v[192:195], v174 offset:35840
	ds_read_b128 v[196:199], v174 offset:36864
	ds_read_b128 v[204:207], v174 offset:37888
	ds_read_b128 v[208:211], v174 offset:38912
	ds_read_b128 v[212:215], v174 offset:39936
	global_load_lds_dwordx4 v[220:221], off
	v_lshl_add_u64 v[220:221], s[62:63], 0, v[162:163]
	s_mov_b32 m0, s69
	s_nop 0
	global_load_lds_dwordx4 v[220:221], off
	s_waitcnt vmcnt(8) lgkmcnt(0)
	s_setprio 1
	s_barrier
	v_mfma_f32_16x16x32_bf16 v[118:121], v[130:133], v[180:183], v[118:121]
	v_mfma_f32_16x16x32_bf16 v[114:117], v[138:141], v[180:183], v[114:117]
	v_mfma_f32_16x16x32_bf16 v[102:105], v[130:133], v[188:191], v[102:105]
	v_mfma_f32_16x16x32_bf16 v[98:101], v[138:141], v[188:191], v[98:101]
	v_mfma_f32_16x16x32_bf16 v[86:89], v[130:133], v[196:199], v[86:89]
	v_mfma_f32_16x16x32_bf16 v[82:85], v[138:141], v[196:199], v[82:85]
	v_mfma_f32_16x16x32_bf16 v[70:73], v[130:133], v[208:211], v[70:73]
	v_mfma_f32_16x16x32_bf16 v[66:69], v[138:141], v[208:211], v[66:69]
	v_mfma_f32_16x16x32_bf16 v[118:121], v[134:137], v[184:187], v[118:121]
	v_mfma_f32_16x16x32_bf16 v[114:117], v[142:145], v[184:187], v[114:117]
	v_mfma_f32_16x16x32_bf16 v[102:105], v[134:137], v[192:195], v[102:105]
	v_mfma_f32_16x16x32_bf16 v[98:101], v[142:145], v[192:195], v[98:101]
	v_mfma_f32_16x16x32_bf16 v[86:89], v[134:137], v[204:207], v[86:89]
	v_mfma_f32_16x16x32_bf16 v[82:85], v[142:145], v[204:207], v[82:85]
	v_mfma_f32_16x16x32_bf16 v[70:73], v[134:137], v[212:215], v[70:73]
	v_mfma_f32_16x16x32_bf16 v[66:69], v[142:145], v[212:215], v[66:69]
	v_mfma_f32_16x16x32_bf16 v[126:129], v[146:149], v[180:183], v[126:129]
	v_mfma_f32_16x16x32_bf16 v[122:125], v[154:157], v[180:183], v[122:125]
	v_mfma_f32_16x16x32_bf16 v[110:113], v[146:149], v[188:191], v[110:113]
	v_mfma_f32_16x16x32_bf16 v[106:109], v[154:157], v[188:191], v[106:109]
	v_mfma_f32_16x16x32_bf16 v[94:97], v[146:149], v[196:199], v[94:97]
	v_mfma_f32_16x16x32_bf16 v[90:93], v[154:157], v[196:199], v[90:93]
	v_mfma_f32_16x16x32_bf16 v[78:81], v[146:149], v[208:211], v[78:81]
	v_mfma_f32_16x16x32_bf16 v[74:77], v[154:157], v[208:211], v[74:77]
	v_mfma_f32_16x16x32_bf16 v[126:129], v[150:153], v[184:187], v[126:129]
	v_mfma_f32_16x16x32_bf16 v[122:125], v[176:179], v[184:187], v[122:125]
	v_mfma_f32_16x16x32_bf16 v[110:113], v[150:153], v[192:195], v[110:113]
	v_mfma_f32_16x16x32_bf16 v[106:109], v[176:179], v[192:195], v[106:109]
	v_mfma_f32_16x16x32_bf16 v[94:97], v[150:153], v[204:207], v[94:97]
	v_mfma_f32_16x16x32_bf16 v[90:93], v[176:179], v[204:207], v[90:93]
	v_mfma_f32_16x16x32_bf16 v[78:81], v[150:153], v[212:215], v[78:81]
	v_mfma_f32_16x16x32_bf16 v[74:77], v[176:179], v[212:215], v[74:77]
	s_barrier
; #define PG8_STAGE(bufoff, gbase, voff) do { _Pragma("unroll") for (int _i = 0; _i < 2; ++_i) \
;         __builtin_amdgcn_global_load_lds((const unsigned*)((const char*)(gbase) + (voff)[_i]), (PG8_LAS unsigned*)(lds + (bufoff) + ldsw + _i * 8192), 16, 0, 0); } while (0)
; #define PG8_LDA(dst, b, h) do { _Pragma("unroll") for (int m = 0; m < 4; ++m) _Pragma("unroll") for (int k = 0; k < 2; ++k) dst[m][k] = *(const PG8_LAS bf16x8*)(lds + PG8_SA(b, h) + aoff + m * 2048 + k * 1024); } while (0)
; #define PG8_MMA(ai, bj, At, Bt) do { __builtin_amdgcn_s_setprio(1); _Pragma("unroll") for (int m = 0; m < 4; ++m) _Pragma("unroll") for (int n = 0; n < 2; ++n) _Pragma("unroll") for (int k = 0; k < 2; ++k) \
;         acc[ai][bj][m][n] = __builtin_amdgcn_mfma_f32_16x16x32_bf16(Bt[n][k], At[m][k], acc[ai][bj][m][n], 0, 0, 0); __builtin_amdgcn_s_setprio(0); } while (0)
; #define PG8_WAIT_V(n) asm volatile("s_waitcnt vmcnt(" #n ")" ::: "memory")
; #define PG8_WAIT_L(n) asm volatile("s_waitcnt lgkmcnt(" #n ")" ::: "memory")
; #define PG8_BAR __builtin_amdgcn_s_barrier()
; #define PG8_SCHED __builtin_amdgcn_sched_barrier(0)
; template <class Epi, class Sched, bool ALIGN_EPI = false, bool SP2 = false>
; __device__ __forceinline__ void gemm_phase(PG8_LAS unsigned char* lds, const Gemm g, const Sched& S, const Epi& E) {
;     ...
;         for (; t < tend; t += 2) {
;     ...
;             PG8_LDA(At, 1, 1); PG8_STAGE(PG8_SB(1, 0), b3, voffB); PG8_STAGE(PG8_SB(1, 1), b3 + hstep, voffB); PG8_STAGEA(PG8_SA(1, 0), a3, 0, last);
;             PG8_WAIT_V(8); PG8_WAIT_L(0); PG8_BAR; PG8_MMA(1, 0, At, B0); PG8_MMA(1, 1, At, B1); PG8_BAR; PG8_SCHED;
	s_setprio 0
	s_add_i32 s62, s95, s65
	v_lshl_add_u64 v[170:171], v[170:171], 0, s[26:27]
	s_mov_b32 m0, s62
	ds_read_b128 v[180:183], v174 offset:49152
	ds_read_b128 v[184:187], v174 offset:50176
	ds_read_b128 v[188:191], v174 offset:51200
	ds_read_b128 v[192:195], v174 offset:52224
	ds_read_b128 v[196:199], v174 offset:53248
	ds_read_b128 v[204:207], v174 offset:54272
	ds_read_b128 v[208:211], v174 offset:55296
	ds_read_b128 v[212:215], v174 offset:56320
	global_load_lds_dwordx4 v[170:171], off
	s_add_i32 m0, s62, 0x2000
	s_add_u32 s58, s58, 0x80080
	v_lshl_add_u64 v[170:171], v[200:201], 0, s[26:27]
	s_addc_u32 s59, s59, 0
	s_add_i32 s62, s96, s65
	global_load_lds_dwordx4 v[170:171], off
	v_lshl_add_u64 v[170:171], s[58:59], 0, v[160:161]
	s_mov_b32 m0, s62
	s_nop 0
	global_load_lds_dwordx4 v[170:171], off
	v_lshl_add_u64 v[170:171], s[58:59], 0, v[164:165]
	s_add_i32 m0, s62, 0x2000
	s_nop 0
	global_load_lds_dwordx4 v[170:171], off
	v_lshl_add_u64 v[170:171], v[216:217], 0, s[26:27]
	s_mov_b32 m0, s76
	s_nop 0
	global_load_lds_dwordx4 v[170:171], off
	v_lshl_add_u64 v[170:171], v[218:219], 0, s[26:27]
	s_mov_b32 m0, s77
	s_nop 0
	global_load_lds_dwordx4 v[170:171], off
	s_waitcnt vmcnt(8) lgkmcnt(0)
	s_setprio 1
	s_barrier
	v_mfma_f32_16x16x32_bf16 v[54:57], v[130:133], v[180:183], v[54:57]
	v_mfma_f32_16x16x32_bf16 v[50:53], v[138:141], v[180:183], v[50:53]
	v_mfma_f32_16x16x32_bf16 v[38:41], v[130:133], v[188:191], v[38:41]
	v_mfma_f32_16x16x32_bf16 v[34:37], v[138:141], v[188:191], v[34:37]
	v_mfma_f32_16x16x32_bf16 v[22:25], v[130:133], v[196:199], v[22:25]
	v_mfma_f32_16x16x32_bf16 v[18:21], v[138:141], v[196:199], v[18:21]
	v_mfma_f32_16x16x32_bf16 v[10:13], v[130:133], v[208:211], v[10:13]
	v_mfma_f32_16x16x32_bf16 v[6:9], v[138:141], v[208:211], v[6:9]
	v_mfma_f32_16x16x32_bf16 v[54:57], v[134:137], v[184:187], v[54:57]
	v_mfma_f32_16x16x32_bf16 v[50:53], v[142:145], v[184:187], v[50:53]
	v_mfma_f32_16x16x32_bf16 v[38:41], v[134:137], v[192:195], v[38:41]
	v_mfma_f32_16x16x32_bf16 v[34:37], v[142:145], v[192:195], v[34:37]
	v_mfma_f32_16x16x32_bf16 v[22:25], v[134:137], v[204:207], v[22:25]
	v_mfma_f32_16x16x32_bf16 v[18:21], v[142:145], v[204:207], v[18:21]
	v_mfma_f32_16x16x32_bf16 v[10:13], v[134:137], v[212:215], v[10:13]
	v_mfma_f32_16x16x32_bf16 v[6:9], v[142:145], v[212:215], v[6:9]
	v_mfma_f32_16x16x32_bf16 v[62:65], v[146:149], v[180:183], v[62:65]
	v_mfma_f32_16x16x32_bf16 v[58:61], v[154:157], v[180:183], v[58:61]
	v_mfma_f32_16x16x32_bf16 v[46:49], v[146:149], v[188:191], v[46:49]
	v_mfma_f32_16x16x32_bf16 v[42:45], v[154:157], v[188:191], v[42:45]
	v_mfma_f32_16x16x32_bf16 v[30:33], v[146:149], v[196:199], v[30:33]
	v_mfma_f32_16x16x32_bf16 v[26:29], v[154:157], v[196:199], v[26:29]
	v_mfma_f32_16x16x32_bf16 v[14:17], v[146:149], v[208:211], v[14:17]
	v_mfma_f32_16x16x32_bf16 v[2:5], v[154:157], v[208:211], v[2:5]
	v_mfma_f32_16x16x32_bf16 v[62:65], v[150:153], v[184:187], v[62:65]
	v_mfma_f32_16x16x32_bf16 v[58:61], v[176:179], v[184:187], v[58:61]
	v_mfma_f32_16x16x32_bf16 v[46:49], v[150:153], v[192:195], v[46:49]
	v_mfma_f32_16x16x32_bf16 v[42:45], v[176:179], v[192:195], v[42:45]
	v_mfma_f32_16x16x32_bf16 v[30:33], v[150:153], v[204:207], v[30:33]
	v_mfma_f32_16x16x32_bf16 v[26:29], v[176:179], v[204:207], v[26:29]
	v_mfma_f32_16x16x32_bf16 v[14:17], v[150:153], v[212:215], v[14:17]
	v_mfma_f32_16x16x32_bf16 v[2:5], v[176:179], v[212:215], v[2:5]
	s_barrier
	s_setprio 0
	s_add_u32 s19, s19, 0x100
	s_addc_u32 s36, s36, 0
	s_add_u32 s37, s37, 0x100
	s_addc_u32 s57, s57, 0
	s_cmp_lt_i32 s56, s18
	s_cbranch_scc1 .LBB0_383

; #define PG8_STAGE(bufoff, gbase, voff) do { _Pragma("unroll") for (int _i = 0; _i < 2; ++_i) \
;         __builtin_amdgcn_global_load_lds((const unsigned*)((const char*)(gbase) + (voff)[_i]), (PG8_LAS unsigned*)(lds + (bufoff) + ldsw + _i * 8192), 16, 0, 0); } while (0)
; #define PG8_LDA(dst, b, h) do { _Pragma("unroll") for (int m = 0; m < 4; ++m) _Pragma("unroll") for (int k = 0; k < 2; ++k) dst[m][k] = *(const PG8_LAS bf16x8*)(lds + PG8_SA(b, h) + aoff + m * 2048 + k * 1024); } while (0)
; #define PG8_LDB(dst, b, h) do { _Pragma("unroll") for (int n = 0; n < 2; ++n) _Pragma("unroll") for (int k = 0; k < 2; ++k) dst[n][k] = *(const PG8_LAS bf16x8*)(lds + PG8_SB(b, h) + boff + n * 2048 + k * 1024); } while (0)
; #define PG8_MMA(ai, bj, At, Bt) do { __builtin_amdgcn_s_setprio(1); _Pragma("unroll") for (int m = 0; m < 4; ++m) _Pragma("unroll") for (int n = 0; n < 2; ++n) _Pragma("unroll") for (int k = 0; k < 2; ++k) \
;         acc[ai][bj][m][n] = __builtin_amdgcn_mfma_f32_16x16x32_bf16(Bt[n][k], At[m][k], acc[ai][bj][m][n], 0, 0, 0); __builtin_amdgcn_s_setprio(0); } while (0)
; #define PG8_WAIT_V(n) asm volatile("s_waitcnt vmcnt(" #n ")" ::: "memory")
; #define PG8_WAIT_L(n) asm volatile("s_waitcnt lgkmcnt(" #n ")" ::: "memory")
; template <class Epi, class Sched, bool ALIGN_EPI = false, bool SP2 = false>
; __device__ __forceinline__ void gemm_phase(PG8_LAS unsigned char* lds, const Gemm g, const Sched& S, const Epi& E) {
;     ...
;             const bool last = (t == nt - 2);
;             const char* a1 = cA + (size_t)(t + 1) * kstep;
;             const char* a2 = last ? nA : cA + (size_t)(t + 2) * kstep; const char* b2 = last ? nB : cB + (size_t)(t + 2) * kstep;
;             const char* a3 = a2 + kstep; const char* b3 = b2 + kstep;
;             if (last && has_next) S.a_ready(nxt);
;             if constexpr (SP2) {
;             PG8_LDB(B0, 0, 0); PG8_LDB(B1, 0, 1); PG8_SCHED; PG8_LDA(At, 0, 0); PG8_STAGEA(PG8_SA(1, 1), a1, 1, false);
;             PG8_WAIT_V(8); PG8_WAIT_L(0); PG8_BAR; PG8_MMA(0, 0, At, B0); PG8_MMA(0, 1, At, B1); PG8_BAR; PG8_SCHED;
;             PG8_LDA(At, 0, 1); PG8_STAGE(PG8_SB(0, 0), b2, voffB); PG8_STAGE(PG8_SB(0, 1), b2 + hstep, voffB); PG8_STAGEA(PG8_SA(0, 0), a2, 0, last);
;             PG8_WAIT_V(8); PG8_WAIT_L(0); PG8_BAR; PG8_MMA(1, 0, At, B0); PG8_MMA(1, 1, At, B1); PG8_BAR; PG8_SCHED;
.LBB0_571:
	v_add_u32_e32 v162, s66, v150
	v_add_u32_e32 v178, s67, v150
	ds_read_b128 v[146:149], v162
	ds_read_b128 v[154:157], v162 offset:1024
	ds_read_b128 v[158:161], v162 offset:2048
	ds_read_b128 v[162:165], v162 offset:3072
	ds_read_b128 v[166:169], v178
	ds_read_b128 v[170:173], v178 offset:1024
	ds_read_b128 v[174:177], v178 offset:2048
	ds_read_b128 v[178:181], v178 offset:3072
	s_add_u32 s52, s50, 0xfff80080
	s_addc_u32 s53, s51, -1
	s_cmp_eq_u32 s49, 28
	s_cselect_b32 s55, s9, s53
	s_cselect_b32 s54, s11, s52
	s_cselect_b32 s53, s36, s43
	s_cselect_b32 s52, s37, s41
	v_lshl_add_u64 v[216:217], s[50:51], 0, v[138:139]
	s_add_i32 m0, s57, 0xc000
	ds_read_b128 v[182:185], v152
	ds_read_b128 v[186:189], v152 offset:1024
	ds_read_b128 v[190:193], v152 offset:2048
	ds_read_b128 v[194:197], v152 offset:3072
	ds_read_b128 v[198:201], v152 offset:4096
	ds_read_b128 v[204:207], v152 offset:5120
	ds_read_b128 v[208:211], v152 offset:6144
	ds_read_b128 v[212:215], v152 offset:7168
	global_load_lds_dwordx4 v[216:217], off
	v_lshl_add_u64 v[216:217], s[50:51], 0, v[140:141]
	s_add_i32 m0, s57, 0xe000
	s_nop 0
	global_load_lds_dwordx4 v[216:217], off
	s_waitcnt vmcnt(8) lgkmcnt(0)
	s_setprio 1
	s_barrier
	v_mfma_f32_16x16x32_bf16 v[126:129], v[146:149], v[182:185], v[126:129]
	v_mfma_f32_16x16x32_bf16 v[122:125], v[158:161], v[182:185], v[122:125]
	v_mfma_f32_16x16x32_bf16 v[110:113], v[146:149], v[190:193], v[110:113]
	v_mfma_f32_16x16x32_bf16 v[106:109], v[158:161], v[190:193], v[106:109]
	v_mfma_f32_16x16x32_bf16 v[94:97], v[146:149], v[198:201], v[94:97]
	v_mfma_f32_16x16x32_bf16 v[90:93], v[158:161], v[198:201], v[90:93]
	v_mfma_f32_16x16x32_bf16 v[78:81], v[146:149], v[208:211], v[78:81]
	v_mfma_f32_16x16x32_bf16 v[74:77], v[158:161], v[208:211], v[74:77]
	v_mfma_f32_16x16x32_bf16 v[126:129], v[154:157], v[186:189], v[126:129]
	v_mfma_f32_16x16x32_bf16 v[122:125], v[162:165], v[186:189], v[122:125]
	v_mfma_f32_16x16x32_bf16 v[110:113], v[154:157], v[194:197], v[110:113]
	v_mfma_f32_16x16x32_bf16 v[106:109], v[162:165], v[194:197], v[106:109]
	v_mfma_f32_16x16x32_bf16 v[94:97], v[154:157], v[204:207], v[94:97]
	v_mfma_f32_16x16x32_bf16 v[90:93], v[162:165], v[204:207], v[90:93]
	v_mfma_f32_16x16x32_bf16 v[78:81], v[154:157], v[212:215], v[78:81]
	v_mfma_f32_16x16x32_bf16 v[74:77], v[162:165], v[212:215], v[74:77]
	v_mfma_f32_16x16x32_bf16 v[118:121], v[166:169], v[182:185], v[118:121]
	v_mfma_f32_16x16x32_bf16 v[114:117], v[174:177], v[182:185], v[114:117]
	v_mfma_f32_16x16x32_bf16 v[102:105], v[166:169], v[190:193], v[102:105]
	v_mfma_f32_16x16x32_bf16 v[98:101], v[174:177], v[190:193], v[98:101]
	v_mfma_f32_16x16x32_bf16 v[86:89], v[166:169], v[198:201], v[86:89]
	v_mfma_f32_16x16x32_bf16 v[82:85], v[174:177], v[198:201], v[82:85]
	v_mfma_f32_16x16x32_bf16 v[70:73], v[166:169], v[208:211], v[70:73]
	v_mfma_f32_16x16x32_bf16 v[66:69], v[174:177], v[208:211], v[66:69]
	v_mfma_f32_16x16x32_bf16 v[118:121], v[170:173], v[186:189], v[118:121]
	v_mfma_f32_16x16x32_bf16 v[114:117], v[178:181], v[186:189], v[114:117]
	v_mfma_f32_16x16x32_bf16 v[102:105], v[170:173], v[194:197], v[102:105]
	v_mfma_f32_16x16x32_bf16 v[98:101], v[178:181], v[194:197], v[98:101]
	v_mfma_f32_16x16x32_bf16 v[86:89], v[170:173], v[204:207], v[86:89]
	v_mfma_f32_16x16x32_bf16 v[82:85], v[178:181], v[204:207], v[82:85]
	v_mfma_f32_16x16x32_bf16 v[70:73], v[170:173], v[212:215], v[70:73]
	v_mfma_f32_16x16x32_bf16 v[66:69], v[178:181], v[212:215], v[66:69]
	s_barrier
	s_setprio 0
	s_add_i32 s69, s66, s56
	v_lshl_add_u64 v[216:217], s[52:53], 0, v[132:133]
	s_mov_b32 m0, s69
	ds_read_b128 v[182:185], v152 offset:16384
	ds_read_b128 v[186:189], v152 offset:17408
	ds_read_b128 v[190:193], v152 offset:18432
	ds_read_b128 v[194:197], v152 offset:19456
	ds_read_b128 v[198:201], v152 offset:20480
	ds_read_b128 v[204:207], v152 offset:21504
	ds_read_b128 v[208:211], v152 offset:22528
	ds_read_b128 v[212:215], v152 offset:23552
	global_load_lds_dwordx4 v[216:217], off
	s_add_i32 m0, s69, 0x2000
	s_add_u32 s74, s52, 0x80000
	v_lshl_add_u64 v[218:219], s[52:53], 0, v[136:137]
	s_addc_u32 s75, s53, 0
	s_add_i32 s69, s67, s56
	global_load_lds_dwordx4 v[218:219], off
	v_lshl_add_u64 v[220:221], s[74:75], 0, v[132:133]
	s_mov_b32 m0, s69
	v_lshl_add_u64 v[222:223], s[54:55], 0, v[134:135]
	global_load_lds_dwordx4 v[220:221], off
	v_lshl_add_u64 v[220:221], s[74:75], 0, v[136:137]
	s_add_i32 m0, s69, 0x2000
	s_nop 0
	global_load_lds_dwordx4 v[220:221], off
	v_lshl_add_u64 v[220:221], s[54:55], 0, v[130:131]
	s_mov_b32 m0, s57
	s_nop 0
	global_load_lds_dwordx4 v[220:221], off
	s_mov_b32 m0, s58
	s_nop 0
	global_load_lds_dwordx4 v[222:223], off
	s_waitcnt vmcnt(8) lgkmcnt(0)
	s_setprio 1
	s_barrier
; #define PG8_LDA(dst, b, h) do { _Pragma("unroll") for (int m = 0; m < 4; ++m) _Pragma("unroll") for (int k = 0; k < 2; ++k) dst[m][k] = *(const PG8_LAS bf16x8*)(lds + PG8_SA(b, h) + aoff + m * 2048 + k * 1024); } while (0)
; #define PG8_LDB(dst, b, h) do { _Pragma("unroll") for (int n = 0; n < 2; ++n) _Pragma("unroll") for (int k = 0; k < 2; ++k) dst[n][k] = *(const PG8_LAS bf16x8*)(lds + PG8_SB(b, h) + boff + n * 2048 + k * 1024); } while (0)
; #define PG8_MMA(ai, bj, At, Bt) do { __builtin_amdgcn_s_setprio(1); _Pragma("unroll") for (int m = 0; m < 4; ++m) _Pragma("unroll") for (int n = 0; n < 2; ++n) _Pragma("unroll") for (int k = 0; k < 2; ++k) \
;         acc[ai][bj][m][n] = __builtin_amdgcn_mfma_f32_16x16x32_bf16(Bt[n][k], At[m][k], acc[ai][bj][m][n], 0, 0, 0); __builtin_amdgcn_s_setprio(0); } while (0)
; #define PG8_WAIT_V(n) asm volatile("s_waitcnt vmcnt(" #n ")" ::: "memory")
; #define PG8_WAIT_L(n) asm volatile("s_waitcnt lgkmcnt(" #n ")" ::: "memory")
; #define PG8_BAR __builtin_amdgcn_s_barrier()
; #define PG8_SCHED __builtin_amdgcn_sched_barrier(0)
; template <class Epi, class Sched, bool ALIGN_EPI = false, bool SP2 = false>
; __device__ __forceinline__ void gemm_phase(PG8_LAS unsigned char* lds, const Gemm g, const Sched& S, const Epi& E) {
;     ...
;             PG8_WAIT_V(8); PG8_WAIT_L(0); PG8_BAR; PG8_MMA(1, 0, At, B0); PG8_MMA(1, 1, At, B1); PG8_BAR; PG8_SCHED;
;             PG8_LDB(B0, 1, 0); PG8_LDB(B1, 1, 1); PG8_SCHED; PG8_LDA(At, 1, 0); PG8_STAGEA(PG8_SA(0, 1), a2, 1, last);
;             PG8_WAIT_V(8); PG8_WAIT_L(0); PG8_BAR; PG8_MMA(0, 0, At, B0); PG8_MMA(0, 1, At, B1); PG8_BAR; PG8_SCHED;
	v_mfma_f32_16x16x32_bf16 v[62:65], v[146:149], v[182:185], v[62:65]
	v_mfma_f32_16x16x32_bf16 v[58:61], v[158:161], v[182:185], v[58:61]
	v_mfma_f32_16x16x32_bf16 v[46:49], v[146:149], v[190:193], v[46:49]
	v_mfma_f32_16x16x32_bf16 v[42:45], v[158:161], v[190:193], v[42:45]
	v_mfma_f32_16x16x32_bf16 v[30:33], v[146:149], v[198:201], v[30:33]
	v_mfma_f32_16x16x32_bf16 v[26:29], v[158:161], v[198:201], v[26:29]
	v_mfma_f32_16x16x32_bf16 v[14:17], v[146:149], v[208:211], v[14:17]
	v_mfma_f32_16x16x32_bf16 v[10:13], v[158:161], v[208:211], v[10:13]
	v_mfma_f32_16x16x32_bf16 v[62:65], v[154:157], v[186:189], v[62:65]
	v_mfma_f32_16x16x32_bf16 v[58:61], v[162:165], v[186:189], v[58:61]
	v_mfma_f32_16x16x32_bf16 v[46:49], v[154:157], v[194:197], v[46:49]
	v_mfma_f32_16x16x32_bf16 v[42:45], v[162:165], v[194:197], v[42:45]
	v_mfma_f32_16x16x32_bf16 v[30:33], v[154:157], v[204:207], v[30:33]
	v_mfma_f32_16x16x32_bf16 v[26:29], v[162:165], v[204:207], v[26:29]
	v_mfma_f32_16x16x32_bf16 v[14:17], v[154:157], v[212:215], v[14:17]
	v_mfma_f32_16x16x32_bf16 v[10:13], v[162:165], v[212:215], v[10:13]
	v_mfma_f32_16x16x32_bf16 v[54:57], v[166:169], v[182:185], v[54:57]
	v_mfma_f32_16x16x32_bf16 v[50:53], v[174:177], v[182:185], v[50:53]
	v_mfma_f32_16x16x32_bf16 v[38:41], v[166:169], v[190:193], v[38:41]
	v_mfma_f32_16x16x32_bf16 v[34:37], v[174:177], v[190:193], v[34:37]
	v_mfma_f32_16x16x32_bf16 v[22:25], v[166:169], v[198:201], v[22:25]
	v_mfma_f32_16x16x32_bf16 v[18:21], v[174:177], v[198:201], v[18:21]
	v_mfma_f32_16x16x32_bf16 v[6:9], v[166:169], v[208:211], v[6:9]
	v_mfma_f32_16x16x32_bf16 v[2:5], v[174:177], v[208:211], v[2:5]
	v_mfma_f32_16x16x32_bf16 v[54:57], v[170:173], v[186:189], v[54:57]
	v_mfma_f32_16x16x32_bf16 v[50:53], v[178:181], v[186:189], v[50:53]
	v_mfma_f32_16x16x32_bf16 v[38:41], v[170:173], v[194:197], v[38:41]
	v_mfma_f32_16x16x32_bf16 v[34:37], v[178:181], v[194:197], v[34:37]
	v_mfma_f32_16x16x32_bf16 v[22:25], v[170:173], v[204:207], v[22:25]
	v_mfma_f32_16x16x32_bf16 v[18:21], v[178:181], v[204:207], v[18:21]
	v_mfma_f32_16x16x32_bf16 v[6:9], v[170:173], v[212:215], v[6:9]
	v_mfma_f32_16x16x32_bf16 v[2:5], v[178:181], v[212:215], v[2:5]
	s_barrier
	s_setprio 0
	s_add_i32 s69, 0, 0x18000
	s_add_i32 s74, 0, 0x1c000
	v_add_u32_e32 v162, s69, v150
	v_add_u32_e32 v178, s74, v150
	ds_read_b128 v[146:149], v162
	ds_read_b128 v[154:157], v162 offset:1024
	ds_read_b128 v[158:161], v162 offset:2048
	ds_read_b128 v[162:165], v162 offset:3072
	ds_read_b128 v[166:169], v178
	ds_read_b128 v[170:173], v178 offset:1024
	ds_read_b128 v[174:177], v178 offset:2048
	ds_read_b128 v[178:181], v178 offset:3072
	s_add_u32 s54, s54, 0x80000
	s_addc_u32 s55, s55, 0
	s_mov_b32 m0, s59
	v_lshl_add_u64 v[224:225], s[54:55], 0, v[130:131]
	ds_read_b128 v[182:185], v152 offset:32768
	ds_read_b128 v[186:189], v152 offset:33792
	ds_read_b128 v[190:193], v152 offset:34816
	ds_read_b128 v[194:197], v152 offset:35840
	ds_read_b128 v[198:201], v152 offset:36864
	ds_read_b128 v[204:207], v152 offset:37888
	ds_read_b128 v[208:211], v152 offset:38912
	ds_read_b128 v[212:215], v152 offset:39936
	global_load_lds_dwordx4 v[224:225], off
	v_lshl_add_u64 v[224:225], s[54:55], 0, v[134:135]
	s_mov_b32 m0, s60
	s_nop 0
	global_load_lds_dwordx4 v[224:225], off
	s_waitcnt vmcnt(8) lgkmcnt(0)
	s_setprio 1
	s_barrier
	v_mfma_f32_16x16x32_bf16 v[126:129], v[146:149], v[182:185], v[126:129]
	v_mfma_f32_16x16x32_bf16 v[122:125], v[158:161], v[182:185], v[122:125]
	v_mfma_f32_16x16x32_bf16 v[110:113], v[146:149], v[190:193], v[110:113]
	v_mfma_f32_16x16x32_bf16 v[106:109], v[158:161], v[190:193], v[106:109]
	v_mfma_f32_16x16x32_bf16 v[94:97], v[146:149], v[198:201], v[94:97]
	v_mfma_f32_16x16x32_bf16 v[90:93], v[158:161], v[198:201], v[90:93]
	v_mfma_f32_16x16x32_bf16 v[78:81], v[146:149], v[208:211], v[78:81]
	v_mfma_f32_16x16x32_bf16 v[74:77], v[158:161], v[208:211], v[74:77]
	v_mfma_f32_16x16x32_bf16 v[126:129], v[154:157], v[186:189], v[126:129]
	v_mfma_f32_16x16x32_bf16 v[122:125], v[162:165], v[186:189], v[122:125]
	v_mfma_f32_16x16x32_bf16 v[110:113], v[154:157], v[194:197], v[110:113]
	v_mfma_f32_16x16x32_bf16 v[106:109], v[162:165], v[194:197], v[106:109]
	v_mfma_f32_16x16x32_bf16 v[94:97], v[154:157], v[204:207], v[94:97]
	v_mfma_f32_16x16x32_bf16 v[90:93], v[162:165], v[204:207], v[90:93]
	v_mfma_f32_16x16x32_bf16 v[78:81], v[154:157], v[212:215], v[78:81]
	v_mfma_f32_16x16x32_bf16 v[74:77], v[162:165], v[212:215], v[74:77]
	v_mfma_f32_16x16x32_bf16 v[118:121], v[166:169], v[182:185], v[118:121]
	v_mfma_f32_16x16x32_bf16 v[114:117], v[174:177], v[182:185], v[114:117]
	v_mfma_f32_16x16x32_bf16 v[102:105], v[166:169], v[190:193], v[102:105]
	v_mfma_f32_16x16x32_bf16 v[98:101], v[174:177], v[190:193], v[98:101]
	v_mfma_f32_16x16x32_bf16 v[86:89], v[166:169], v[198:201], v[86:89]
	v_mfma_f32_16x16x32_bf16 v[82:85], v[174:177], v[198:201], v[82:85]
	v_mfma_f32_16x16x32_bf16 v[70:73], v[166:169], v[208:211], v[70:73]
	v_mfma_f32_16x16x32_bf16 v[66:69], v[174:177], v[208:211], v[66:69]
	v_mfma_f32_16x16x32_bf16 v[118:121], v[170:173], v[186:189], v[118:121]
	v_mfma_f32_16x16x32_bf16 v[114:117], v[178:181], v[186:189], v[114:117]
	v_mfma_f32_16x16x32_bf16 v[102:105], v[170:173], v[194:197], v[102:105]
	v_mfma_f32_16x16x32_bf16 v[98:101], v[178:181], v[194:197], v[98:101]
	v_mfma_f32_16x16x32_bf16 v[86:89], v[170:173], v[204:207], v[86:89]
	v_mfma_f32_16x16x32_bf16 v[82:85], v[178:181], v[204:207], v[82:85]
	v_mfma_f32_16x16x32_bf16 v[70:73], v[170:173], v[212:215], v[70:73]
	v_mfma_f32_16x16x32_bf16 v[66:69], v[178:181], v[212:215], v[66:69]
	s_barrier
; #define PG8_STAGE(bufoff, gbase, voff) do { _Pragma("unroll") for (int _i = 0; _i < 2; ++_i) \
;         __builtin_amdgcn_global_load_lds((const unsigned*)((const char*)(gbase) + (voff)[_i]), (PG8_LAS unsigned*)(lds + (bufoff) + ldsw + _i * 8192), 16, 0, 0); } while (0)
; #define PG8_LDA(dst, b, h) do { _Pragma("unroll") for (int m = 0; m < 4; ++m) _Pragma("unroll") for (int k = 0; k < 2; ++k) dst[m][k] = *(const PG8_LAS bf16x8*)(lds + PG8_SA(b, h) + aoff + m * 2048 + k * 1024); } while (0)
; #define PG8_MMA(ai, bj, At, Bt) do { __builtin_amdgcn_s_setprio(1); _Pragma("unroll") for (int m = 0; m < 4; ++m) _Pragma("unroll") for (int n = 0; n < 2; ++n) _Pragma("unroll") for (int k = 0; k < 2; ++k) \
;         acc[ai][bj][m][n] = __builtin_amdgcn_mfma_f32_16x16x32_bf16(Bt[n][k], At[m][k], acc[ai][bj][m][n], 0, 0, 0); __builtin_amdgcn_s_setprio(0); } while (0)
; #define PG8_WAIT_V(n) asm volatile("s_waitcnt vmcnt(" #n ")" ::: "memory")
; #define PG8_WAIT_L(n) asm volatile("s_waitcnt lgkmcnt(" #n ")" ::: "memory")
; #define PG8_BAR __builtin_amdgcn_s_barrier()
; #define PG8_SCHED __builtin_amdgcn_sched_barrier(0)
; template <class Epi, class Sched, bool ALIGN_EPI = false, bool SP2 = false>
; __device__ __forceinline__ void gemm_phase(PG8_LAS unsigned char* lds, const Gemm g, const Sched& S, const Epi& E) {
;     ...
;             PG8_LDA(At, 1, 1); PG8_STAGE(PG8_SB(1, 0), b3, voffB); PG8_STAGE(PG8_SB(1, 1), b3 + hstep, voffB); PG8_STAGEA(PG8_SA(1, 0), a3, 0, last);
;             PG8_WAIT_V(8); PG8_WAIT_L(0); PG8_BAR; PG8_MMA(1, 0, At, B0); PG8_MMA(1, 1, At, B1); PG8_BAR; PG8_SCHED;
;     ...
;         if constexpr (ALIGN_EPI) { if (wr == 0) PG8_BAR; }
	s_setprio 0
	s_add_i32 s54, s69, s56
	v_lshl_add_u64 v[216:217], v[216:217], 0, s[26:27]
	s_mov_b32 m0, s54
	ds_read_b128 v[182:185], v152 offset:49152
	ds_read_b128 v[186:189], v152 offset:50176
	ds_read_b128 v[190:193], v152 offset:51200
	ds_read_b128 v[194:197], v152 offset:52224
	ds_read_b128 v[198:201], v152 offset:53248
	ds_read_b128 v[204:207], v152 offset:54272
	ds_read_b128 v[208:211], v152 offset:55296
	ds_read_b128 v[212:215], v152 offset:56320
	global_load_lds_dwordx4 v[216:217], off
	s_add_i32 m0, s54, 0x2000
	s_add_u32 s52, s52, 0x80080
	v_lshl_add_u64 v[216:217], v[218:219], 0, s[26:27]
	s_addc_u32 s53, s53, 0
	s_add_i32 s54, s74, s56
	global_load_lds_dwordx4 v[216:217], off
	v_lshl_add_u64 v[216:217], s[52:53], 0, v[132:133]
	s_mov_b32 m0, s54
	s_nop 0
	global_load_lds_dwordx4 v[216:217], off
	v_lshl_add_u64 v[216:217], s[52:53], 0, v[136:137]
	s_add_i32 m0, s54, 0x2000
	s_nop 0
	global_load_lds_dwordx4 v[216:217], off
	v_lshl_add_u64 v[216:217], v[220:221], 0, s[26:27]
	s_mov_b32 m0, s62
	s_nop 0
	global_load_lds_dwordx4 v[216:217], off
	v_lshl_add_u64 v[216:217], v[222:223], 0, s[26:27]
	s_mov_b32 m0, s63
	s_nop 0
	global_load_lds_dwordx4 v[216:217], off
	s_waitcnt vmcnt(8) lgkmcnt(0)
	s_setprio 1
	s_barrier
	v_mfma_f32_16x16x32_bf16 v[62:65], v[146:149], v[182:185], v[62:65]
	v_mfma_f32_16x16x32_bf16 v[58:61], v[158:161], v[182:185], v[58:61]
	v_mfma_f32_16x16x32_bf16 v[46:49], v[146:149], v[190:193], v[46:49]
	v_mfma_f32_16x16x32_bf16 v[42:45], v[158:161], v[190:193], v[42:45]
	v_mfma_f32_16x16x32_bf16 v[30:33], v[146:149], v[198:201], v[30:33]
	v_mfma_f32_16x16x32_bf16 v[26:29], v[158:161], v[198:201], v[26:29]
	v_mfma_f32_16x16x32_bf16 v[14:17], v[146:149], v[208:211], v[14:17]
	v_mfma_f32_16x16x32_bf16 v[10:13], v[158:161], v[208:211], v[10:13]
	v_mfma_f32_16x16x32_bf16 v[62:65], v[154:157], v[186:189], v[62:65]
	v_mfma_f32_16x16x32_bf16 v[58:61], v[162:165], v[186:189], v[58:61]
	v_mfma_f32_16x16x32_bf16 v[46:49], v[154:157], v[194:197], v[46:49]
	v_mfma_f32_16x16x32_bf16 v[42:45], v[162:165], v[194:197], v[42:45]
	v_mfma_f32_16x16x32_bf16 v[30:33], v[154:157], v[204:207], v[30:33]
	v_mfma_f32_16x16x32_bf16 v[26:29], v[162:165], v[204:207], v[26:29]
	v_mfma_f32_16x16x32_bf16 v[14:17], v[154:157], v[212:215], v[14:17]
	v_mfma_f32_16x16x32_bf16 v[10:13], v[162:165], v[212:215], v[10:13]
	v_mfma_f32_16x16x32_bf16 v[54:57], v[166:169], v[182:185], v[54:57]
	v_mfma_f32_16x16x32_bf16 v[50:53], v[174:177], v[182:185], v[50:53]
	v_mfma_f32_16x16x32_bf16 v[38:41], v[166:169], v[190:193], v[38:41]
	v_mfma_f32_16x16x32_bf16 v[34:37], v[174:177], v[190:193], v[34:37]
	v_mfma_f32_16x16x32_bf16 v[22:25], v[166:169], v[198:201], v[22:25]
	v_mfma_f32_16x16x32_bf16 v[18:21], v[174:177], v[198:201], v[18:21]
	v_mfma_f32_16x16x32_bf16 v[6:9], v[166:169], v[208:211], v[6:9]
	v_mfma_f32_16x16x32_bf16 v[2:5], v[174:177], v[208:211], v[2:5]
	v_mfma_f32_16x16x32_bf16 v[54:57], v[170:173], v[186:189], v[54:57]
	v_mfma_f32_16x16x32_bf16 v[50:53], v[178:181], v[186:189], v[50:53]
	v_mfma_f32_16x16x32_bf16 v[38:41], v[170:173], v[194:197], v[38:41]
	v_mfma_f32_16x16x32_bf16 v[34:37], v[178:181], v[194:197], v[34:37]
	v_mfma_f32_16x16x32_bf16 v[22:25], v[170:173], v[204:207], v[22:25]
	v_mfma_f32_16x16x32_bf16 v[18:21], v[178:181], v[204:207], v[18:21]
	v_mfma_f32_16x16x32_bf16 v[6:9], v[170:173], v[212:215], v[6:9]
	v_mfma_f32_16x16x32_bf16 v[2:5], v[178:181], v[212:215], v[2:5]
	s_barrier
	s_setprio 0
	s_add_i32 s49, s49, 2
	s_add_u32 s50, s50, 0x100
	s_addc_u32 s51, s51, 0
	s_add_u32 s41, s41, 0x100
	s_addc_u32 s43, s43, 0
	s_cmp_gt_u32 s49, 29
	s_cbranch_scc0 .LBB0_571
	s_and_b64 vcc, exec, s[38:39]
	s_cbranch_vccz .LBB0_574
	s_barrier

; #define PG8_STAGE(bufoff, gbase, voff) do { _Pragma("unroll") for (int _i = 0; _i < 2; ++_i) \
;         __builtin_amdgcn_global_load_lds((const unsigned*)((const char*)(gbase) + (voff)[_i]), (PG8_LAS unsigned*)(lds + (bufoff) + ldsw + _i * 8192), 16, 0, 0); } while (0)
; #define PG8_LDA(dst, b, h) do { _Pragma("unroll") for (int m = 0; m < 4; ++m) _Pragma("unroll") for (int k = 0; k < 2; ++k) dst[m][k] = *(const PG8_LAS bf16x8*)(lds + PG8_SA(b, h) + aoff + m * 2048 + k * 1024); } while (0)
; #define PG8_LDB(dst, b, h) do { _Pragma("unroll") for (int n = 0; n < 2; ++n) _Pragma("unroll") for (int k = 0; k < 2; ++k) dst[n][k] = *(const PG8_LAS bf16x8*)(lds + PG8_SB(b, h) + boff + n * 2048 + k * 1024); } while (0)
; #define PG8_MMA(ai, bj, At, Bt) do { __builtin_amdgcn_s_setprio(1); _Pragma("unroll") for (int m = 0; m < 4; ++m) _Pragma("unroll") for (int n = 0; n < 2; ++n) _Pragma("unroll") for (int k = 0; k < 2; ++k) \
;         acc[ai][bj][m][n] = __builtin_amdgcn_mfma_f32_16x16x32_bf16(Bt[n][k], At[m][k], acc[ai][bj][m][n], 0, 0, 0); __builtin_amdgcn_s_setprio(0); } while (0)
; #define PG8_WAIT_V(n) asm volatile("s_waitcnt vmcnt(" #n ")" ::: "memory")
; #define PG8_WAIT_L(n) asm volatile("s_waitcnt lgkmcnt(" #n ")" ::: "memory")
; template <class Epi, class Sched, bool ALIGN_EPI = false, bool SP2 = false>
; __device__ __forceinline__ void gemm_phase(PG8_LAS unsigned char* lds, const Gemm g, const Sched& S, const Epi& E) {
;     ...
;             const bool last = (t == nt - 2);
;             const char* a1 = cA + (size_t)(t + 1) * kstep;
;             const char* a2 = last ? nA : cA + (size_t)(t + 2) * kstep; const char* b2 = last ? nB : cB + (size_t)(t + 2) * kstep;
;             const char* a3 = a2 + kstep; const char* b3 = b2 + kstep;
;             if (last && has_next) S.a_ready(nxt);
;             if constexpr (SP2) {
;             PG8_LDB(B0, 0, 0); PG8_LDB(B1, 0, 1); PG8_SCHED; PG8_LDA(At, 0, 0); PG8_STAGEA(PG8_SA(1, 1), a1, 1, false);
;             PG8_WAIT_V(8); PG8_WAIT_L(0); PG8_BAR; PG8_MMA(0, 0, At, B0); PG8_MMA(0, 1, At, B1); PG8_BAR; PG8_SCHED;
;             PG8_LDA(At, 0, 1); PG8_STAGE(PG8_SB(0, 0), b2, voffB); PG8_STAGE(PG8_SB(0, 1), b2 + hstep, voffB); PG8_STAGEA(PG8_SA(0, 0), a2, 0, last);
;             PG8_WAIT_V(8); PG8_WAIT_L(0); PG8_BAR; PG8_MMA(1, 0, At, B0); PG8_MMA(1, 1, At, B1); PG8_BAR; PG8_SCHED;
.LBB0_792:
	s_add_u32 s6, s12, 0x100
	v_add_u32_e32 v134, s84, v152
	s_addc_u32 s7, s13, 0
	ds_read_b128 v[162:165], v134
	ds_read_b128 v[166:169], v134 offset:1024
	ds_read_b128 v[170:173], v134 offset:2048
	ds_read_b128 v[174:177], v134 offset:3072
	v_add_u32_e32 v134, s85, v152
	s_add_u32 s10, s16, s12
	ds_read_b128 v[178:181], v134
	ds_read_b128 v[182:185], v134 offset:1024
	ds_read_b128 v[186:189], v134 offset:2048
	ds_read_b128 v[190:193], v134 offset:3072
	s_addc_u32 s11, s17, s13
	s_cmpk_eq_i32 s12, 0xf00
	s_cselect_b64 vcc, -1, 0
	s_and_b64 s[8:9], vcc, exec
	s_cselect_b32 s36, 0, s6
	s_cselect_b32 s27, 0, s7
	s_cselect_b32 s8, s18, s10
	s_cselect_b32 s9, s15, s11
	s_add_u32 s10, s42, s36
	s_addc_u32 s11, s43, s27
	v_lshl_add_u64 v[228:229], v[142:143], 0, s[12:13]
	s_add_i32 m0, s77, 0xc000
	ds_read_b128 v[194:197], v156
	ds_read_b128 v[198:201], v156 offset:1024
	ds_read_b128 v[204:207], v156 offset:2048
	ds_read_b128 v[208:211], v156 offset:3072
	ds_read_b128 v[212:215], v156 offset:4096
	ds_read_b128 v[216:219], v156 offset:5120
	ds_read_b128 v[220:223], v156 offset:6144
	ds_read_b128 v[224:227], v156 offset:7168
	global_load_lds_dwordx4 v[228:229], off
	v_lshl_add_u64 v[228:229], v[144:145], 0, s[12:13]
	s_add_i32 m0, s77, 0xe000
	s_nop 0
	global_load_lds_dwordx4 v[228:229], off
	s_waitcnt vmcnt(8) lgkmcnt(0)
	s_setprio 1
	s_barrier
	v_mfma_f32_16x16x32_bf16 v[126:129], v[162:165], v[194:197], v[126:129]
	v_mfma_f32_16x16x32_bf16 v[118:121], v[170:173], v[194:197], v[118:121]
	v_mfma_f32_16x16x32_bf16 v[110:113], v[162:165], v[204:207], v[110:113]
	v_mfma_f32_16x16x32_bf16 v[102:105], v[170:173], v[204:207], v[102:105]
	v_mfma_f32_16x16x32_bf16 v[94:97], v[162:165], v[212:215], v[94:97]
	v_mfma_f32_16x16x32_bf16 v[86:89], v[170:173], v[212:215], v[86:89]
	v_mfma_f32_16x16x32_bf16 v[78:81], v[162:165], v[220:223], v[78:81]
	v_mfma_f32_16x16x32_bf16 v[70:73], v[170:173], v[220:223], v[70:73]
	v_mfma_f32_16x16x32_bf16 v[126:129], v[166:169], v[198:201], v[126:129]
	v_mfma_f32_16x16x32_bf16 v[118:121], v[174:177], v[198:201], v[118:121]
	v_mfma_f32_16x16x32_bf16 v[110:113], v[166:169], v[208:211], v[110:113]
	v_mfma_f32_16x16x32_bf16 v[102:105], v[174:177], v[208:211], v[102:105]
	v_mfma_f32_16x16x32_bf16 v[94:97], v[166:169], v[216:219], v[94:97]
	v_mfma_f32_16x16x32_bf16 v[86:89], v[174:177], v[216:219], v[86:89]
	v_mfma_f32_16x16x32_bf16 v[78:81], v[166:169], v[224:227], v[78:81]
	v_mfma_f32_16x16x32_bf16 v[70:73], v[174:177], v[224:227], v[70:73]
	v_mfma_f32_16x16x32_bf16 v[122:125], v[178:181], v[194:197], v[122:125]
	v_mfma_f32_16x16x32_bf16 v[114:117], v[186:189], v[194:197], v[114:117]
	v_mfma_f32_16x16x32_bf16 v[106:109], v[178:181], v[204:207], v[106:109]
	v_mfma_f32_16x16x32_bf16 v[98:101], v[186:189], v[204:207], v[98:101]
	v_mfma_f32_16x16x32_bf16 v[90:93], v[178:181], v[212:215], v[90:93]
	v_mfma_f32_16x16x32_bf16 v[82:85], v[186:189], v[212:215], v[82:85]
	v_mfma_f32_16x16x32_bf16 v[74:77], v[178:181], v[220:223], v[74:77]
	v_mfma_f32_16x16x32_bf16 v[66:69], v[186:189], v[220:223], v[66:69]
	v_mfma_f32_16x16x32_bf16 v[122:125], v[182:185], v[198:201], v[122:125]
	v_mfma_f32_16x16x32_bf16 v[114:117], v[190:193], v[198:201], v[114:117]
	v_mfma_f32_16x16x32_bf16 v[106:109], v[182:185], v[208:211], v[106:109]
	v_mfma_f32_16x16x32_bf16 v[98:101], v[190:193], v[208:211], v[98:101]
	v_mfma_f32_16x16x32_bf16 v[90:93], v[182:185], v[216:219], v[90:93]
	v_mfma_f32_16x16x32_bf16 v[82:85], v[190:193], v[216:219], v[82:85]
	v_mfma_f32_16x16x32_bf16 v[74:77], v[182:185], v[224:227], v[74:77]
	v_mfma_f32_16x16x32_bf16 v[66:69], v[190:193], v[224:227], v[66:69]
	s_barrier
	s_setprio 0
	s_add_i32 s12, s84, s76
	v_lshl_add_u64 v[228:229], s[8:9], 0, v[130:131]
	s_mov_b32 m0, s12
	ds_read_b128 v[194:197], v156 offset:16384
	ds_read_b128 v[198:201], v156 offset:17408
	ds_read_b128 v[204:207], v156 offset:18432
	ds_read_b128 v[208:211], v156 offset:19456
	ds_read_b128 v[212:215], v156 offset:20480
	ds_read_b128 v[216:219], v156 offset:21504
	ds_read_b128 v[220:223], v156 offset:22528
	ds_read_b128 v[224:227], v156 offset:23552
	global_load_lds_dwordx4 v[228:229], off
	s_add_i32 m0, s12, 0x2000
	s_add_u32 s12, s8, 0x80000
	v_lshl_add_u64 v[230:231], s[8:9], 0, v[132:133]
	s_addc_u32 s13, s9, 0
	s_add_i32 s27, s85, s76
	global_load_lds_dwordx4 v[230:231], off
	v_lshl_add_u64 v[232:233], s[12:13], 0, v[130:131]
	s_mov_b32 m0, s27
	v_cndmask_b32_e32 v134, v146, v157, vcc
	global_load_lds_dwordx4 v[232:233], off
	v_lshl_add_u64 v[232:233], s[12:13], 0, v[132:133]
	s_add_i32 m0, s27, 0x2000
	s_nop 0
	global_load_lds_dwordx4 v[232:233], off
	s_mov_b32 m0, s77
	v_lshl_add_u64 v[232:233], s[10:11], 0, v[134:135]
	global_load_lds_dwordx4 v134, s[10:11]
	v_cndmask_b32_e32 v134, v136, v158, vcc
	s_mov_b32 m0, s78
	v_lshl_add_u64 v[234:235], s[10:11], 0, v[134:135]
	global_load_lds_dwordx4 v134, s[10:11]
	s_waitcnt vmcnt(8) lgkmcnt(0)
	s_setprio 1
	s_barrier
; #define PG8_STAGE(bufoff, gbase, voff) do { _Pragma("unroll") for (int _i = 0; _i < 2; ++_i) \
;         __builtin_amdgcn_global_load_lds((const unsigned*)((const char*)(gbase) + (voff)[_i]), (PG8_LAS unsigned*)(lds + (bufoff) + ldsw + _i * 8192), 16, 0, 0); } while (0)
; #define PG8_LDA(dst, b, h) do { _Pragma("unroll") for (int m = 0; m < 4; ++m) _Pragma("unroll") for (int k = 0; k < 2; ++k) dst[m][k] = *(const PG8_LAS bf16x8*)(lds + PG8_SA(b, h) + aoff + m * 2048 + k * 1024); } while (0)
; #define PG8_LDB(dst, b, h) do { _Pragma("unroll") for (int n = 0; n < 2; ++n) _Pragma("unroll") for (int k = 0; k < 2; ++k) dst[n][k] = *(const PG8_LAS bf16x8*)(lds + PG8_SB(b, h) + boff + n * 2048 + k * 1024); } while (0)
; #define PG8_MMA(ai, bj, At, Bt) do { __builtin_amdgcn_s_setprio(1); _Pragma("unroll") for (int m = 0; m < 4; ++m) _Pragma("unroll") for (int n = 0; n < 2; ++n) _Pragma("unroll") for (int k = 0; k < 2; ++k) \
;         acc[ai][bj][m][n] = __builtin_amdgcn_mfma_f32_16x16x32_bf16(Bt[n][k], At[m][k], acc[ai][bj][m][n], 0, 0, 0); __builtin_amdgcn_s_setprio(0); } while (0)
; #define PG8_WAIT_V(n) asm volatile("s_waitcnt vmcnt(" #n ")" ::: "memory")
; #define PG8_WAIT_L(n) asm volatile("s_waitcnt lgkmcnt(" #n ")" ::: "memory")
; #define PG8_BAR __builtin_amdgcn_s_barrier()
; #define PG8_SCHED __builtin_amdgcn_sched_barrier(0)
; template <class Epi, class Sched, bool ALIGN_EPI = false, bool SP2 = false>
; __device__ __forceinline__ void gemm_phase(PG8_LAS unsigned char* lds, const Gemm g, const Sched& S, const Epi& E) {
;     ...
;             PG8_WAIT_V(8); PG8_WAIT_L(0); PG8_BAR; PG8_MMA(1, 0, At, B0); PG8_MMA(1, 1, At, B1); PG8_BAR; PG8_SCHED;
;             PG8_LDB(B0, 1, 0); PG8_LDB(B1, 1, 1); PG8_SCHED; PG8_LDA(At, 1, 0); PG8_STAGEA(PG8_SA(0, 1), a2, 1, last);
;             PG8_WAIT_V(8); PG8_WAIT_L(0); PG8_BAR; PG8_MMA(0, 0, At, B0); PG8_MMA(0, 1, At, B1); PG8_BAR; PG8_SCHED;
;             PG8_LDA(At, 1, 1); PG8_STAGE(PG8_SB(1, 0), b3, voffB); PG8_STAGE(PG8_SB(1, 1), b3 + hstep, voffB); PG8_STAGEA(PG8_SA(1, 0), a3, 0, last);
	v_mfma_f32_16x16x32_bf16 v[62:65], v[162:165], v[194:197], v[62:65]
	v_mfma_f32_16x16x32_bf16 v[54:57], v[170:173], v[194:197], v[54:57]
	v_mfma_f32_16x16x32_bf16 v[46:49], v[162:165], v[204:207], v[46:49]
	v_mfma_f32_16x16x32_bf16 v[38:41], v[170:173], v[204:207], v[38:41]
	v_mfma_f32_16x16x32_bf16 v[30:33], v[162:165], v[212:215], v[30:33]
	v_mfma_f32_16x16x32_bf16 v[22:25], v[170:173], v[212:215], v[22:25]
	v_mfma_f32_16x16x32_bf16 v[14:17], v[162:165], v[220:223], v[14:17]
	v_mfma_f32_16x16x32_bf16 v[6:9], v[170:173], v[220:223], v[6:9]
	v_mfma_f32_16x16x32_bf16 v[62:65], v[166:169], v[198:201], v[62:65]
	v_mfma_f32_16x16x32_bf16 v[54:57], v[174:177], v[198:201], v[54:57]
	v_mfma_f32_16x16x32_bf16 v[46:49], v[166:169], v[208:211], v[46:49]
	v_mfma_f32_16x16x32_bf16 v[38:41], v[174:177], v[208:211], v[38:41]
	v_mfma_f32_16x16x32_bf16 v[30:33], v[166:169], v[216:219], v[30:33]
	v_mfma_f32_16x16x32_bf16 v[22:25], v[174:177], v[216:219], v[22:25]
	v_mfma_f32_16x16x32_bf16 v[14:17], v[166:169], v[224:227], v[14:17]
	v_mfma_f32_16x16x32_bf16 v[6:9], v[174:177], v[224:227], v[6:9]
	v_mfma_f32_16x16x32_bf16 v[58:61], v[178:181], v[194:197], v[58:61]
	v_mfma_f32_16x16x32_bf16 v[50:53], v[186:189], v[194:197], v[50:53]
	v_mfma_f32_16x16x32_bf16 v[42:45], v[178:181], v[204:207], v[42:45]
	v_mfma_f32_16x16x32_bf16 v[34:37], v[186:189], v[204:207], v[34:37]
	v_mfma_f32_16x16x32_bf16 v[26:29], v[178:181], v[212:215], v[26:29]
	v_mfma_f32_16x16x32_bf16 v[18:21], v[186:189], v[212:215], v[18:21]
	v_mfma_f32_16x16x32_bf16 v[10:13], v[178:181], v[220:223], v[10:13]
	v_mfma_f32_16x16x32_bf16 v[2:5], v[186:189], v[220:223], v[2:5]
	v_mfma_f32_16x16x32_bf16 v[58:61], v[182:185], v[198:201], v[58:61]
	v_mfma_f32_16x16x32_bf16 v[50:53], v[190:193], v[198:201], v[50:53]
	v_mfma_f32_16x16x32_bf16 v[42:45], v[182:185], v[208:211], v[42:45]
	v_mfma_f32_16x16x32_bf16 v[34:37], v[190:193], v[208:211], v[34:37]
	v_mfma_f32_16x16x32_bf16 v[26:29], v[182:185], v[216:219], v[26:29]
	v_mfma_f32_16x16x32_bf16 v[18:21], v[190:193], v[216:219], v[18:21]
	v_mfma_f32_16x16x32_bf16 v[10:13], v[182:185], v[224:227], v[10:13]
	v_mfma_f32_16x16x32_bf16 v[2:5], v[190:193], v[224:227], v[2:5]
	s_barrier
	s_setprio 0
	s_add_i32 s12, 0, 0x18000
	v_add_u32_e32 v134, s12, v152
	s_add_i32 s13, 0, 0x1c000
	ds_read_b128 v[162:165], v134
	ds_read_b128 v[166:169], v134 offset:1024
	ds_read_b128 v[170:173], v134 offset:2048
	ds_read_b128 v[174:177], v134 offset:3072
	v_add_u32_e32 v134, s13, v152
	ds_read_b128 v[178:181], v134
	ds_read_b128 v[182:185], v134 offset:1024
	ds_read_b128 v[186:189], v134 offset:2048
	ds_read_b128 v[190:193], v134 offset:3072
	s_mov_b32 m0, s79
	v_cndmask_b32_e32 v134, v138, v159, vcc
	ds_read_b128 v[194:197], v156 offset:32768
	ds_read_b128 v[198:201], v156 offset:33792
	ds_read_b128 v[204:207], v156 offset:34816
	ds_read_b128 v[208:211], v156 offset:35840
	ds_read_b128 v[212:215], v156 offset:36864
	ds_read_b128 v[216:219], v156 offset:37888
	ds_read_b128 v[220:223], v156 offset:38912
	ds_read_b128 v[224:227], v156 offset:39936
	global_load_lds_dwordx4 v134, s[10:11]
	v_cndmask_b32_e32 v134, v140, v160, vcc
	s_mov_b32 m0, s80
	s_nop 0
	global_load_lds_dwordx4 v134, s[10:11]
	s_waitcnt vmcnt(8) lgkmcnt(0)
	s_setprio 1
	s_barrier
	v_mfma_f32_16x16x32_bf16 v[126:129], v[162:165], v[194:197], v[126:129]
	v_mfma_f32_16x16x32_bf16 v[118:121], v[170:173], v[194:197], v[118:121]
	v_mfma_f32_16x16x32_bf16 v[110:113], v[162:165], v[204:207], v[110:113]
	v_mfma_f32_16x16x32_bf16 v[102:105], v[170:173], v[204:207], v[102:105]
	v_mfma_f32_16x16x32_bf16 v[94:97], v[162:165], v[212:215], v[94:97]
	v_mfma_f32_16x16x32_bf16 v[86:89], v[170:173], v[212:215], v[86:89]
	v_mfma_f32_16x16x32_bf16 v[78:81], v[162:165], v[220:223], v[78:81]
	v_mfma_f32_16x16x32_bf16 v[70:73], v[170:173], v[220:223], v[70:73]
	v_mfma_f32_16x16x32_bf16 v[126:129], v[166:169], v[198:201], v[126:129]
	v_mfma_f32_16x16x32_bf16 v[118:121], v[174:177], v[198:201], v[118:121]
	v_mfma_f32_16x16x32_bf16 v[110:113], v[166:169], v[208:211], v[110:113]
	v_mfma_f32_16x16x32_bf16 v[102:105], v[174:177], v[208:211], v[102:105]
	v_mfma_f32_16x16x32_bf16 v[94:97], v[166:169], v[216:219], v[94:97]
	v_mfma_f32_16x16x32_bf16 v[86:89], v[174:177], v[216:219], v[86:89]
	v_mfma_f32_16x16x32_bf16 v[78:81], v[166:169], v[224:227], v[78:81]
	v_mfma_f32_16x16x32_bf16 v[70:73], v[174:177], v[224:227], v[70:73]
	v_mfma_f32_16x16x32_bf16 v[122:125], v[178:181], v[194:197], v[122:125]
	v_mfma_f32_16x16x32_bf16 v[114:117], v[186:189], v[194:197], v[114:117]
	v_mfma_f32_16x16x32_bf16 v[106:109], v[178:181], v[204:207], v[106:109]
	v_mfma_f32_16x16x32_bf16 v[98:101], v[186:189], v[204:207], v[98:101]
	v_mfma_f32_16x16x32_bf16 v[90:93], v[178:181], v[212:215], v[90:93]
	v_mfma_f32_16x16x32_bf16 v[82:85], v[186:189], v[212:215], v[82:85]
	v_mfma_f32_16x16x32_bf16 v[74:77], v[178:181], v[220:223], v[74:77]
	v_mfma_f32_16x16x32_bf16 v[66:69], v[186:189], v[220:223], v[66:69]
	v_mfma_f32_16x16x32_bf16 v[122:125], v[182:185], v[198:201], v[122:125]
	v_mfma_f32_16x16x32_bf16 v[114:117], v[190:193], v[198:201], v[114:117]
	v_mfma_f32_16x16x32_bf16 v[106:109], v[182:185], v[208:211], v[106:109]
	v_mfma_f32_16x16x32_bf16 v[98:101], v[190:193], v[208:211], v[98:101]
	v_mfma_f32_16x16x32_bf16 v[90:93], v[182:185], v[216:219], v[90:93]
	v_mfma_f32_16x16x32_bf16 v[82:85], v[190:193], v[216:219], v[82:85]
	v_mfma_f32_16x16x32_bf16 v[74:77], v[182:185], v[224:227], v[74:77]
	v_mfma_f32_16x16x32_bf16 v[66:69], v[190:193], v[224:227], v[66:69]
	s_barrier
; #define PG8_STAGE(bufoff, gbase, voff) do { _Pragma("unroll") for (int _i = 0; _i < 2; ++_i) \
;         __builtin_amdgcn_global_load_lds((const unsigned*)((const char*)(gbase) + (voff)[_i]), (PG8_LAS unsigned*)(lds + (bufoff) + ldsw + _i * 8192), 16, 0, 0); } while (0)
; #define PG8_LDA(dst, b, h) do { _Pragma("unroll") for (int m = 0; m < 4; ++m) _Pragma("unroll") for (int k = 0; k < 2; ++k) dst[m][k] = *(const PG8_LAS bf16x8*)(lds + PG8_SA(b, h) + aoff + m * 2048 + k * 1024); } while (0)
; #define PG8_MMA(ai, bj, At, Bt) do { __builtin_amdgcn_s_setprio(1); _Pragma("unroll") for (int m = 0; m < 4; ++m) _Pragma("unroll") for (int n = 0; n < 2; ++n) _Pragma("unroll") for (int k = 0; k < 2; ++k) \
;         acc[ai][bj][m][n] = __builtin_amdgcn_mfma_f32_16x16x32_bf16(Bt[n][k], At[m][k], acc[ai][bj][m][n], 0, 0, 0); __builtin_amdgcn_s_setprio(0); } while (0)
; #define PG8_WAIT_V(n) asm volatile("s_waitcnt vmcnt(" #n ")" ::: "memory")
; #define PG8_WAIT_L(n) asm volatile("s_waitcnt lgkmcnt(" #n ")" ::: "memory")
; #define PG8_BAR __builtin_amdgcn_s_barrier()
; #define PG8_SCHED __builtin_amdgcn_sched_barrier(0)
; template <class Epi, class Sched, bool ALIGN_EPI = false, bool SP2 = false>
; __device__ __forceinline__ void gemm_phase(PG8_LAS unsigned char* lds, const Gemm g, const Sched& S, const Epi& E) {
;     ...
;             PG8_LDA(At, 1, 1); PG8_STAGE(PG8_SB(1, 0), b3, voffB); PG8_STAGE(PG8_SB(1, 1), b3 + hstep, voffB); PG8_STAGEA(PG8_SA(1, 0), a3, 0, last);
;             PG8_WAIT_V(8); PG8_WAIT_L(0); PG8_BAR; PG8_MMA(1, 0, At, B0); PG8_MMA(1, 1, At, B1); PG8_BAR; PG8_SCHED;
;     ...
;         if constexpr (ALIGN_EPI) { if (wr == 0) PG8_BAR; }
	s_setprio 0
	s_add_i32 s10, s12, s76
	v_lshl_add_u64 v[228:229], v[228:229], 0, s[52:53]
	s_mov_b32 m0, s10
	ds_read_b128 v[194:197], v156 offset:49152
	ds_read_b128 v[198:201], v156 offset:50176
	ds_read_b128 v[204:207], v156 offset:51200
	ds_read_b128 v[208:211], v156 offset:52224
	ds_read_b128 v[212:215], v156 offset:53248
	ds_read_b128 v[216:219], v156 offset:54272
	ds_read_b128 v[220:223], v156 offset:55296
	ds_read_b128 v[224:227], v156 offset:56320
	global_load_lds_dwordx4 v[228:229], off
	s_add_i32 m0, s10, 0x2000
	s_add_u32 s8, s8, 0x80080
	v_lshl_add_u64 v[228:229], v[230:231], 0, s[52:53]
	s_addc_u32 s9, s9, 0
	s_add_i32 s10, s13, s76
	global_load_lds_dwordx4 v[228:229], off
	v_lshl_add_u64 v[228:229], s[8:9], 0, v[130:131]
	s_mov_b32 m0, s10
	s_nop 0
	global_load_lds_dwordx4 v[228:229], off
	v_lshl_add_u64 v[228:229], s[8:9], 0, v[132:133]
	s_add_i32 m0, s10, 0x2000
	s_nop 0
	global_load_lds_dwordx4 v[228:229], off
	v_lshl_add_u64 v[228:229], v[232:233], 0, s[52:53]
	s_mov_b32 m0, s81
	s_nop 0
	global_load_lds_dwordx4 v[228:229], off
	v_lshl_add_u64 v[228:229], v[234:235], 0, s[52:53]
	s_mov_b32 m0, s82
	s_nop 0
	global_load_lds_dwordx4 v[228:229], off
	s_waitcnt vmcnt(8) lgkmcnt(0)
	s_setprio 1
	s_barrier
	v_mfma_f32_16x16x32_bf16 v[62:65], v[162:165], v[194:197], v[62:65]
	v_mfma_f32_16x16x32_bf16 v[54:57], v[170:173], v[194:197], v[54:57]
	v_mfma_f32_16x16x32_bf16 v[46:49], v[162:165], v[204:207], v[46:49]
	v_mfma_f32_16x16x32_bf16 v[38:41], v[170:173], v[204:207], v[38:41]
	v_mfma_f32_16x16x32_bf16 v[30:33], v[162:165], v[212:215], v[30:33]
	v_mfma_f32_16x16x32_bf16 v[22:25], v[170:173], v[212:215], v[22:25]
	v_mfma_f32_16x16x32_bf16 v[14:17], v[162:165], v[220:223], v[14:17]
	v_mfma_f32_16x16x32_bf16 v[6:9], v[170:173], v[220:223], v[6:9]
	v_mfma_f32_16x16x32_bf16 v[62:65], v[166:169], v[198:201], v[62:65]
	v_mfma_f32_16x16x32_bf16 v[54:57], v[174:177], v[198:201], v[54:57]
	v_mfma_f32_16x16x32_bf16 v[46:49], v[166:169], v[208:211], v[46:49]
	v_mfma_f32_16x16x32_bf16 v[38:41], v[174:177], v[208:211], v[38:41]
	v_mfma_f32_16x16x32_bf16 v[30:33], v[166:169], v[216:219], v[30:33]
	v_mfma_f32_16x16x32_bf16 v[22:25], v[174:177], v[216:219], v[22:25]
	v_mfma_f32_16x16x32_bf16 v[14:17], v[166:169], v[224:227], v[14:17]
	v_mfma_f32_16x16x32_bf16 v[6:9], v[174:177], v[224:227], v[6:9]
	v_mfma_f32_16x16x32_bf16 v[58:61], v[178:181], v[194:197], v[58:61]
	v_mfma_f32_16x16x32_bf16 v[50:53], v[186:189], v[194:197], v[50:53]
	v_mfma_f32_16x16x32_bf16 v[42:45], v[178:181], v[204:207], v[42:45]
	v_mfma_f32_16x16x32_bf16 v[34:37], v[186:189], v[204:207], v[34:37]
	v_mfma_f32_16x16x32_bf16 v[26:29], v[178:181], v[212:215], v[26:29]
	v_mfma_f32_16x16x32_bf16 v[18:21], v[186:189], v[212:215], v[18:21]
	v_mfma_f32_16x16x32_bf16 v[10:13], v[178:181], v[220:223], v[10:13]
	v_mfma_f32_16x16x32_bf16 v[2:5], v[186:189], v[220:223], v[2:5]
	v_mfma_f32_16x16x32_bf16 v[58:61], v[182:185], v[198:201], v[58:61]
	v_mfma_f32_16x16x32_bf16 v[50:53], v[190:193], v[198:201], v[50:53]
	v_mfma_f32_16x16x32_bf16 v[42:45], v[182:185], v[208:211], v[42:45]
	v_mfma_f32_16x16x32_bf16 v[34:37], v[190:193], v[208:211], v[34:37]
	v_mfma_f32_16x16x32_bf16 v[26:29], v[182:185], v[216:219], v[26:29]
	v_mfma_f32_16x16x32_bf16 v[18:21], v[190:193], v[216:219], v[18:21]
	v_mfma_f32_16x16x32_bf16 v[10:13], v[182:185], v[224:227], v[10:13]
	v_mfma_f32_16x16x32_bf16 v[2:5], v[190:193], v[224:227], v[2:5]
	s_barrier
	s_setprio 0
	s_add_i32 s19, s19, 2
	s_cmp_gt_u32 s19, 29
	s_mov_b64 s[12:13], s[6:7]
	s_cbranch_scc0 .LBB0_792
	s_and_b64 vcc, exec, s[56:57]
	s_cbranch_vccz .LBB0_795
	s_barrier

; #define PG8_STAGE(bufoff, gbase, voff) do { _Pragma("unroll") for (int _i = 0; _i < 2; ++_i) \
;         __builtin_amdgcn_global_load_lds((const unsigned*)((const char*)(gbase) + (voff)[_i]), (PG8_LAS unsigned*)(lds + (bufoff) + ldsw + _i * 8192), 16, 0, 0); } while (0)
; #define PG8_LDA(dst, b, h) do { _Pragma("unroll") for (int m = 0; m < 4; ++m) _Pragma("unroll") for (int k = 0; k < 2; ++k) dst[m][k] = *(const PG8_LAS bf16x8*)(lds + PG8_SA(b, h) + aoff + m * 2048 + k * 1024); } while (0)
; #define PG8_LDB(dst, b, h) do { _Pragma("unroll") for (int n = 0; n < 2; ++n) _Pragma("unroll") for (int k = 0; k < 2; ++k) dst[n][k] = *(const PG8_LAS bf16x8*)(lds + PG8_SB(b, h) + boff + n * 2048 + k * 1024); } while (0)
; #define PG8_MMA(ai, bj, At, Bt) do { __builtin_amdgcn_s_setprio(1); _Pragma("unroll") for (int m = 0; m < 4; ++m) _Pragma("unroll") for (int n = 0; n < 2; ++n) _Pragma("unroll") for (int k = 0; k < 2; ++k) \
;         acc[ai][bj][m][n] = __builtin_amdgcn_mfma_f32_16x16x32_bf16(Bt[n][k], At[m][k], acc[ai][bj][m][n], 0, 0, 0); __builtin_amdgcn_s_setprio(0); } while (0)
; #define PG8_WAIT_V(n) asm volatile("s_waitcnt vmcnt(" #n ")" ::: "memory")
; #define PG8_WAIT_L(n) asm volatile("s_waitcnt lgkmcnt(" #n ")" ::: "memory")
; template <class Epi, class Sched, bool ALIGN_EPI = false, bool SP2 = false>
; __device__ __forceinline__ void gemm_phase(PG8_LAS unsigned char* lds, const Gemm g, const Sched& S, const Epi& E) {
;     ...
;             const bool last = (t == nt - 2);
;             const char* a1 = cA + (size_t)(t + 1) * kstep;
;             const char* a2 = last ? nA : cA + (size_t)(t + 2) * kstep; const char* b2 = last ? nB : cB + (size_t)(t + 2) * kstep;
;             const char* a3 = a2 + kstep; const char* b3 = b2 + kstep;
;             if (last && has_next) S.a_ready(nxt);
;             if constexpr (SP2) {
;             PG8_LDB(B0, 0, 0); PG8_LDB(B1, 0, 1); PG8_SCHED; PG8_LDA(At, 0, 0); PG8_STAGEA(PG8_SA(1, 1), a1, 1, false);
;             PG8_WAIT_V(8); PG8_WAIT_L(0); PG8_BAR; PG8_MMA(0, 0, At, B0); PG8_MMA(0, 1, At, B1); PG8_BAR; PG8_SCHED;
;             PG8_LDA(At, 0, 1); PG8_STAGE(PG8_SB(0, 0), b2, voffB); PG8_STAGE(PG8_SB(0, 1), b2 + hstep, voffB); PG8_STAGEA(PG8_SA(0, 0), a2, 0, last);
;             PG8_WAIT_V(8); PG8_WAIT_L(0); PG8_BAR; PG8_MMA(1, 0, At, B0); PG8_MMA(1, 1, At, B1); PG8_BAR; PG8_SCHED;
.LBB0_927:
	v_add_u32_e32 v147, s76, v142
	ds_read_b128 v[148:151], v147
	ds_read_b128 v[152:155], v147 offset:1024
	ds_read_b128 v[156:159], v147 offset:2048
	ds_read_b128 v[160:163], v147 offset:3072
	v_add_u32_e32 v147, s77, v142
	ds_read_b128 v[164:167], v147
	ds_read_b128 v[168:171], v147 offset:1024
	ds_read_b128 v[172:175], v147 offset:2048
	ds_read_b128 v[176:179], v147 offset:3072
	s_add_u32 s60, s58, 0xfffe0080
	s_addc_u32 s61, s59, -1
	s_cmp_eq_u32 s83, 4
	s_cselect_b32 s63, s9, s61
	s_cselect_b32 s62, s11, s60
	s_cselect_b32 s61, s36, s49
	s_cselect_b32 s60, s37, s47
	v_lshl_add_u64 v[200:201], s[58:59], 0, v[138:139]
	s_add_i32 m0, s57, 0xc000
	ds_read_b128 v[180:183], v146
	ds_read_b128 v[184:187], v146 offset:1024
	ds_read_b128 v[188:191], v146 offset:2048
	ds_read_b128 v[192:195], v146 offset:3072
	ds_read_b128 v[196:199], v146 offset:4096
	ds_read_b128 v[204:207], v146 offset:5120
	ds_read_b128 v[208:211], v146 offset:6144
	ds_read_b128 v[212:215], v146 offset:7168
	global_load_lds_dwordx4 v[200:201], off
	v_lshl_add_u64 v[200:201], s[58:59], 0, v[140:141]
	s_add_i32 m0, s57, 0xe000
	s_nop 0
	global_load_lds_dwordx4 v[200:201], off
	s_waitcnt vmcnt(8) lgkmcnt(0)
	s_setprio 1
	s_barrier
	v_mfma_f32_16x16x32_bf16 v[122:125], v[148:151], v[180:183], v[122:125]
	v_mfma_f32_16x16x32_bf16 v[126:129], v[156:159], v[180:183], v[126:129]
	v_mfma_f32_16x16x32_bf16 v[106:109], v[148:151], v[188:191], v[106:109]
	v_mfma_f32_16x16x32_bf16 v[110:113], v[156:159], v[188:191], v[110:113]
	v_mfma_f32_16x16x32_bf16 v[90:93], v[148:151], v[196:199], v[90:93]
	v_mfma_f32_16x16x32_bf16 v[94:97], v[156:159], v[196:199], v[94:97]
	v_mfma_f32_16x16x32_bf16 v[74:77], v[148:151], v[208:211], v[74:77]
	v_mfma_f32_16x16x32_bf16 v[78:81], v[156:159], v[208:211], v[78:81]
	v_mfma_f32_16x16x32_bf16 v[122:125], v[152:155], v[184:187], v[122:125]
	v_mfma_f32_16x16x32_bf16 v[126:129], v[160:163], v[184:187], v[126:129]
	v_mfma_f32_16x16x32_bf16 v[106:109], v[152:155], v[192:195], v[106:109]
	v_mfma_f32_16x16x32_bf16 v[110:113], v[160:163], v[192:195], v[110:113]
	v_mfma_f32_16x16x32_bf16 v[90:93], v[152:155], v[204:207], v[90:93]
	v_mfma_f32_16x16x32_bf16 v[94:97], v[160:163], v[204:207], v[94:97]
	v_mfma_f32_16x16x32_bf16 v[74:77], v[152:155], v[212:215], v[74:77]
	v_mfma_f32_16x16x32_bf16 v[78:81], v[160:163], v[212:215], v[78:81]
	v_mfma_f32_16x16x32_bf16 v[114:117], v[164:167], v[180:183], v[114:117]
	v_mfma_f32_16x16x32_bf16 v[118:121], v[172:175], v[180:183], v[118:121]
	v_mfma_f32_16x16x32_bf16 v[98:101], v[164:167], v[188:191], v[98:101]
	v_mfma_f32_16x16x32_bf16 v[102:105], v[172:175], v[188:191], v[102:105]
	v_mfma_f32_16x16x32_bf16 v[82:85], v[164:167], v[196:199], v[82:85]
	v_mfma_f32_16x16x32_bf16 v[86:89], v[172:175], v[196:199], v[86:89]
	v_mfma_f32_16x16x32_bf16 v[66:69], v[164:167], v[208:211], v[66:69]
	v_mfma_f32_16x16x32_bf16 v[70:73], v[172:175], v[208:211], v[70:73]
	v_mfma_f32_16x16x32_bf16 v[114:117], v[168:171], v[184:187], v[114:117]
	v_mfma_f32_16x16x32_bf16 v[118:121], v[176:179], v[184:187], v[118:121]
	v_mfma_f32_16x16x32_bf16 v[98:101], v[168:171], v[192:195], v[98:101]
	v_mfma_f32_16x16x32_bf16 v[102:105], v[176:179], v[192:195], v[102:105]
	v_mfma_f32_16x16x32_bf16 v[82:85], v[168:171], v[204:207], v[82:85]
	v_mfma_f32_16x16x32_bf16 v[86:89], v[176:179], v[204:207], v[86:89]
	v_mfma_f32_16x16x32_bf16 v[66:69], v[168:171], v[212:215], v[66:69]
	v_mfma_f32_16x16x32_bf16 v[70:73], v[176:179], v[212:215], v[70:73]
	s_barrier
	s_setprio 0
	s_add_i32 s84, s76, s65
	v_lshl_add_u64 v[200:201], s[60:61], 0, v[132:133]
	s_mov_b32 m0, s84
	ds_read_b128 v[180:183], v146 offset:16384
	ds_read_b128 v[184:187], v146 offset:17408
	ds_read_b128 v[188:191], v146 offset:18432
	ds_read_b128 v[192:195], v146 offset:19456
	ds_read_b128 v[196:199], v146 offset:20480
	ds_read_b128 v[204:207], v146 offset:21504
	ds_read_b128 v[208:211], v146 offset:22528
	ds_read_b128 v[212:215], v146 offset:23552
	global_load_lds_dwordx4 v[200:201], off
	s_add_i32 m0, s84, 0x2000
	s_add_u32 s84, s60, 0x20000
	v_lshl_add_u64 v[216:217], s[60:61], 0, v[136:137]
	s_addc_u32 s85, s61, 0
	s_add_i32 s86, s77, s65
	global_load_lds_dwordx4 v[216:217], off
	v_lshl_add_u64 v[218:219], s[84:85], 0, v[132:133]
	s_mov_b32 m0, s86
	v_lshl_add_u64 v[220:221], s[62:63], 0, v[134:135]
	global_load_lds_dwordx4 v[218:219], off
	v_lshl_add_u64 v[218:219], s[84:85], 0, v[136:137]
	s_add_i32 m0, s86, 0x2000
	s_nop 0
	global_load_lds_dwordx4 v[218:219], off
	v_lshl_add_u64 v[218:219], s[62:63], 0, v[130:131]
	s_mov_b32 m0, s57
	s_nop 0
	global_load_lds_dwordx4 v[218:219], off
	s_mov_b32 m0, s66
	s_nop 0
	global_load_lds_dwordx4 v[220:221], off
	s_waitcnt vmcnt(8) lgkmcnt(0)
	s_setprio 1
	s_barrier
; #define PG8_LDA(dst, b, h) do { _Pragma("unroll") for (int m = 0; m < 4; ++m) _Pragma("unroll") for (int k = 0; k < 2; ++k) dst[m][k] = *(const PG8_LAS bf16x8*)(lds + PG8_SA(b, h) + aoff + m * 2048 + k * 1024); } while (0)
; #define PG8_LDB(dst, b, h) do { _Pragma("unroll") for (int n = 0; n < 2; ++n) _Pragma("unroll") for (int k = 0; k < 2; ++k) dst[n][k] = *(const PG8_LAS bf16x8*)(lds + PG8_SB(b, h) + boff + n * 2048 + k * 1024); } while (0)
; #define PG8_MMA(ai, bj, At, Bt) do { __builtin_amdgcn_s_setprio(1); _Pragma("unroll") for (int m = 0; m < 4; ++m) _Pragma("unroll") for (int n = 0; n < 2; ++n) _Pragma("unroll") for (int k = 0; k < 2; ++k) \
;         acc[ai][bj][m][n] = __builtin_amdgcn_mfma_f32_16x16x32_bf16(Bt[n][k], At[m][k], acc[ai][bj][m][n], 0, 0, 0); __builtin_amdgcn_s_setprio(0); } while (0)
; #define PG8_WAIT_V(n) asm volatile("s_waitcnt vmcnt(" #n ")" ::: "memory")
; #define PG8_WAIT_L(n) asm volatile("s_waitcnt lgkmcnt(" #n ")" ::: "memory")
; #define PG8_BAR __builtin_amdgcn_s_barrier()
; #define PG8_SCHED __builtin_amdgcn_sched_barrier(0)
; template <class Epi, class Sched, bool ALIGN_EPI = false, bool SP2 = false>
; __device__ __forceinline__ void gemm_phase(PG8_LAS unsigned char* lds, const Gemm g, const Sched& S, const Epi& E) {
;     ...
;             PG8_WAIT_V(8); PG8_WAIT_L(0); PG8_BAR; PG8_MMA(1, 0, At, B0); PG8_MMA(1, 1, At, B1); PG8_BAR; PG8_SCHED;
;             PG8_LDB(B0, 1, 0); PG8_LDB(B1, 1, 1); PG8_SCHED; PG8_LDA(At, 1, 0); PG8_STAGEA(PG8_SA(0, 1), a2, 1, last);
;             PG8_WAIT_V(8); PG8_WAIT_L(0); PG8_BAR; PG8_MMA(0, 0, At, B0); PG8_MMA(0, 1, At, B1); PG8_BAR; PG8_SCHED;
	v_mfma_f32_16x16x32_bf16 v[58:61], v[148:151], v[180:183], v[58:61]
	v_mfma_f32_16x16x32_bf16 v[62:65], v[156:159], v[180:183], v[62:65]
	v_mfma_f32_16x16x32_bf16 v[42:45], v[148:151], v[188:191], v[42:45]
	v_mfma_f32_16x16x32_bf16 v[46:49], v[156:159], v[188:191], v[46:49]
	v_mfma_f32_16x16x32_bf16 v[26:29], v[148:151], v[196:199], v[26:29]
	v_mfma_f32_16x16x32_bf16 v[30:33], v[156:159], v[196:199], v[30:33]
	v_mfma_f32_16x16x32_bf16 v[10:13], v[148:151], v[208:211], v[10:13]
	v_mfma_f32_16x16x32_bf16 v[14:17], v[156:159], v[208:211], v[14:17]
	v_mfma_f32_16x16x32_bf16 v[58:61], v[152:155], v[184:187], v[58:61]
	v_mfma_f32_16x16x32_bf16 v[62:65], v[160:163], v[184:187], v[62:65]
	v_mfma_f32_16x16x32_bf16 v[42:45], v[152:155], v[192:195], v[42:45]
	v_mfma_f32_16x16x32_bf16 v[46:49], v[160:163], v[192:195], v[46:49]
	v_mfma_f32_16x16x32_bf16 v[26:29], v[152:155], v[204:207], v[26:29]
	v_mfma_f32_16x16x32_bf16 v[30:33], v[160:163], v[204:207], v[30:33]
	v_mfma_f32_16x16x32_bf16 v[10:13], v[152:155], v[212:215], v[10:13]
	v_mfma_f32_16x16x32_bf16 v[14:17], v[160:163], v[212:215], v[14:17]
	v_mfma_f32_16x16x32_bf16 v[50:53], v[164:167], v[180:183], v[50:53]
	v_mfma_f32_16x16x32_bf16 v[54:57], v[172:175], v[180:183], v[54:57]
	v_mfma_f32_16x16x32_bf16 v[34:37], v[164:167], v[188:191], v[34:37]
	v_mfma_f32_16x16x32_bf16 v[38:41], v[172:175], v[188:191], v[38:41]
	v_mfma_f32_16x16x32_bf16 v[18:21], v[164:167], v[196:199], v[18:21]
	v_mfma_f32_16x16x32_bf16 v[22:25], v[172:175], v[196:199], v[22:25]
	v_mfma_f32_16x16x32_bf16 v[6:9], v[164:167], v[208:211], v[6:9]
	v_mfma_f32_16x16x32_bf16 v[2:5], v[172:175], v[208:211], v[2:5]
	v_mfma_f32_16x16x32_bf16 v[50:53], v[168:171], v[184:187], v[50:53]
	v_mfma_f32_16x16x32_bf16 v[54:57], v[176:179], v[184:187], v[54:57]
	v_mfma_f32_16x16x32_bf16 v[34:37], v[168:171], v[192:195], v[34:37]
	v_mfma_f32_16x16x32_bf16 v[38:41], v[176:179], v[192:195], v[38:41]
	v_mfma_f32_16x16x32_bf16 v[18:21], v[168:171], v[204:207], v[18:21]
	v_mfma_f32_16x16x32_bf16 v[22:25], v[176:179], v[204:207], v[22:25]
	v_mfma_f32_16x16x32_bf16 v[6:9], v[168:171], v[212:215], v[6:9]
	v_mfma_f32_16x16x32_bf16 v[2:5], v[176:179], v[212:215], v[2:5]
	s_barrier
	s_setprio 0
	s_add_i32 s84, 0, 0x18000
	v_add_u32_e32 v147, s84, v142
	s_add_i32 s85, 0, 0x1c000
	ds_read_b128 v[148:151], v147
	ds_read_b128 v[152:155], v147 offset:1024
	ds_read_b128 v[156:159], v147 offset:2048
	ds_read_b128 v[160:163], v147 offset:3072
	v_add_u32_e32 v147, s85, v142
	ds_read_b128 v[164:167], v147
	ds_read_b128 v[168:171], v147 offset:1024
	ds_read_b128 v[172:175], v147 offset:2048
	ds_read_b128 v[176:179], v147 offset:3072
	s_add_u32 s62, s62, 0x20000
	s_addc_u32 s63, s63, 0
	s_mov_b32 m0, s67
	v_lshl_add_u64 v[222:223], s[62:63], 0, v[130:131]
	ds_read_b128 v[180:183], v146 offset:32768
	ds_read_b128 v[184:187], v146 offset:33792
	ds_read_b128 v[188:191], v146 offset:34816
	ds_read_b128 v[192:195], v146 offset:35840
	ds_read_b128 v[196:199], v146 offset:36864
	ds_read_b128 v[204:207], v146 offset:37888
	ds_read_b128 v[208:211], v146 offset:38912
	ds_read_b128 v[212:215], v146 offset:39936
	global_load_lds_dwordx4 v[222:223], off
	v_lshl_add_u64 v[222:223], s[62:63], 0, v[134:135]
	s_mov_b32 m0, s68
	s_nop 0
	global_load_lds_dwordx4 v[222:223], off
	s_waitcnt vmcnt(8) lgkmcnt(0)
	s_setprio 1
	s_barrier
	v_mfma_f32_16x16x32_bf16 v[122:125], v[148:151], v[180:183], v[122:125]
	v_mfma_f32_16x16x32_bf16 v[126:129], v[156:159], v[180:183], v[126:129]
	v_mfma_f32_16x16x32_bf16 v[106:109], v[148:151], v[188:191], v[106:109]
	v_mfma_f32_16x16x32_bf16 v[110:113], v[156:159], v[188:191], v[110:113]
	v_mfma_f32_16x16x32_bf16 v[90:93], v[148:151], v[196:199], v[90:93]
	v_mfma_f32_16x16x32_bf16 v[94:97], v[156:159], v[196:199], v[94:97]
	v_mfma_f32_16x16x32_bf16 v[74:77], v[148:151], v[208:211], v[74:77]
	v_mfma_f32_16x16x32_bf16 v[78:81], v[156:159], v[208:211], v[78:81]
	v_mfma_f32_16x16x32_bf16 v[122:125], v[152:155], v[184:187], v[122:125]
	v_mfma_f32_16x16x32_bf16 v[126:129], v[160:163], v[184:187], v[126:129]
	v_mfma_f32_16x16x32_bf16 v[106:109], v[152:155], v[192:195], v[106:109]
	v_mfma_f32_16x16x32_bf16 v[110:113], v[160:163], v[192:195], v[110:113]
	v_mfma_f32_16x16x32_bf16 v[90:93], v[152:155], v[204:207], v[90:93]
	v_mfma_f32_16x16x32_bf16 v[94:97], v[160:163], v[204:207], v[94:97]
	v_mfma_f32_16x16x32_bf16 v[74:77], v[152:155], v[212:215], v[74:77]
	v_mfma_f32_16x16x32_bf16 v[78:81], v[160:163], v[212:215], v[78:81]
	v_mfma_f32_16x16x32_bf16 v[114:117], v[164:167], v[180:183], v[114:117]
	v_mfma_f32_16x16x32_bf16 v[118:121], v[172:175], v[180:183], v[118:121]
	v_mfma_f32_16x16x32_bf16 v[98:101], v[164:167], v[188:191], v[98:101]
	v_mfma_f32_16x16x32_bf16 v[102:105], v[172:175], v[188:191], v[102:105]
	v_mfma_f32_16x16x32_bf16 v[82:85], v[164:167], v[196:199], v[82:85]
	v_mfma_f32_16x16x32_bf16 v[86:89], v[172:175], v[196:199], v[86:89]
	v_mfma_f32_16x16x32_bf16 v[66:69], v[164:167], v[208:211], v[66:69]
	v_mfma_f32_16x16x32_bf16 v[70:73], v[172:175], v[208:211], v[70:73]
	v_mfma_f32_16x16x32_bf16 v[114:117], v[168:171], v[184:187], v[114:117]
	v_mfma_f32_16x16x32_bf16 v[118:121], v[176:179], v[184:187], v[118:121]
	v_mfma_f32_16x16x32_bf16 v[98:101], v[168:171], v[192:195], v[98:101]
	v_mfma_f32_16x16x32_bf16 v[102:105], v[176:179], v[192:195], v[102:105]
	v_mfma_f32_16x16x32_bf16 v[82:85], v[168:171], v[204:207], v[82:85]
	v_mfma_f32_16x16x32_bf16 v[86:89], v[176:179], v[204:207], v[86:89]
	v_mfma_f32_16x16x32_bf16 v[66:69], v[168:171], v[212:215], v[66:69]
	v_mfma_f32_16x16x32_bf16 v[70:73], v[176:179], v[212:215], v[70:73]
	s_barrier
; #define PG8_STAGE(bufoff, gbase, voff) do { _Pragma("unroll") for (int _i = 0; _i < 2; ++_i) \
;         __builtin_amdgcn_global_load_lds((const unsigned*)((const char*)(gbase) + (voff)[_i]), (PG8_LAS unsigned*)(lds + (bufoff) + ldsw + _i * 8192), 16, 0, 0); } while (0)
; #define PG8_LDA(dst, b, h) do { _Pragma("unroll") for (int m = 0; m < 4; ++m) _Pragma("unroll") for (int k = 0; k < 2; ++k) dst[m][k] = *(const PG8_LAS bf16x8*)(lds + PG8_SA(b, h) + aoff + m * 2048 + k * 1024); } while (0)
; #define PG8_MMA(ai, bj, At, Bt) do { __builtin_amdgcn_s_setprio(1); _Pragma("unroll") for (int m = 0; m < 4; ++m) _Pragma("unroll") for (int n = 0; n < 2; ++n) _Pragma("unroll") for (int k = 0; k < 2; ++k) \
;         acc[ai][bj][m][n] = __builtin_amdgcn_mfma_f32_16x16x32_bf16(Bt[n][k], At[m][k], acc[ai][bj][m][n], 0, 0, 0); __builtin_amdgcn_s_setprio(0); } while (0)
; #define PG8_WAIT_V(n) asm volatile("s_waitcnt vmcnt(" #n ")" ::: "memory")
; #define PG8_WAIT_L(n) asm volatile("s_waitcnt lgkmcnt(" #n ")" ::: "memory")
; #define PG8_BAR __builtin_amdgcn_s_barrier()
; #define PG8_SCHED __builtin_amdgcn_sched_barrier(0)
; template <class Epi, class Sched, bool ALIGN_EPI = false, bool SP2 = false>
; __device__ __forceinline__ void gemm_phase(PG8_LAS unsigned char* lds, const Gemm g, const Sched& S, const Epi& E) {
;     ...
;             PG8_LDA(At, 1, 1); PG8_STAGE(PG8_SB(1, 0), b3, voffB); PG8_STAGE(PG8_SB(1, 1), b3 + hstep, voffB); PG8_STAGEA(PG8_SA(1, 0), a3, 0, last);
;             PG8_WAIT_V(8); PG8_WAIT_L(0); PG8_BAR; PG8_MMA(1, 0, At, B0); PG8_MMA(1, 1, At, B1); PG8_BAR; PG8_SCHED;
;     ...
;         if constexpr (ALIGN_EPI) { if (wr == 0) PG8_BAR; }
	s_setprio 0
	s_add_i32 s62, s84, s65
	v_lshl_add_u64 v[200:201], v[200:201], 0, s[18:19]
	s_mov_b32 m0, s62
	ds_read_b128 v[180:183], v146 offset:49152
	ds_read_b128 v[184:187], v146 offset:50176
	ds_read_b128 v[188:191], v146 offset:51200
	ds_read_b128 v[192:195], v146 offset:52224
	ds_read_b128 v[196:199], v146 offset:53248
	ds_read_b128 v[204:207], v146 offset:54272
	ds_read_b128 v[208:211], v146 offset:55296
	ds_read_b128 v[212:215], v146 offset:56320
	global_load_lds_dwordx4 v[200:201], off
	s_add_i32 m0, s62, 0x2000
	s_add_u32 s60, s60, 0x20080
	v_lshl_add_u64 v[200:201], v[216:217], 0, s[18:19]
	s_addc_u32 s61, s61, 0
	s_add_i32 s62, s85, s65
	global_load_lds_dwordx4 v[200:201], off
	v_lshl_add_u64 v[200:201], s[60:61], 0, v[132:133]
	s_mov_b32 m0, s62
	s_nop 0
	global_load_lds_dwordx4 v[200:201], off
	v_lshl_add_u64 v[200:201], s[60:61], 0, v[136:137]
	s_add_i32 m0, s62, 0x2000
	s_nop 0
	global_load_lds_dwordx4 v[200:201], off
	v_lshl_add_u64 v[200:201], v[218:219], 0, s[18:19]
	s_mov_b32 m0, s69
	s_nop 0
	global_load_lds_dwordx4 v[200:201], off
	v_lshl_add_u64 v[200:201], v[220:221], 0, s[18:19]
	s_mov_b32 m0, s74
	s_nop 0
	global_load_lds_dwordx4 v[200:201], off
	s_waitcnt vmcnt(8) lgkmcnt(0)
	s_setprio 1
	s_barrier
	v_mfma_f32_16x16x32_bf16 v[58:61], v[148:151], v[180:183], v[58:61]
	v_mfma_f32_16x16x32_bf16 v[62:65], v[156:159], v[180:183], v[62:65]
	v_mfma_f32_16x16x32_bf16 v[42:45], v[148:151], v[188:191], v[42:45]
	v_mfma_f32_16x16x32_bf16 v[46:49], v[156:159], v[188:191], v[46:49]
	v_mfma_f32_16x16x32_bf16 v[26:29], v[148:151], v[196:199], v[26:29]
	v_mfma_f32_16x16x32_bf16 v[30:33], v[156:159], v[196:199], v[30:33]
	v_mfma_f32_16x16x32_bf16 v[10:13], v[148:151], v[208:211], v[10:13]
	v_mfma_f32_16x16x32_bf16 v[14:17], v[156:159], v[208:211], v[14:17]
	v_mfma_f32_16x16x32_bf16 v[58:61], v[152:155], v[184:187], v[58:61]
	v_mfma_f32_16x16x32_bf16 v[62:65], v[160:163], v[184:187], v[62:65]
	v_mfma_f32_16x16x32_bf16 v[42:45], v[152:155], v[192:195], v[42:45]
	v_mfma_f32_16x16x32_bf16 v[46:49], v[160:163], v[192:195], v[46:49]
	v_mfma_f32_16x16x32_bf16 v[26:29], v[152:155], v[204:207], v[26:29]
	v_mfma_f32_16x16x32_bf16 v[30:33], v[160:163], v[204:207], v[30:33]
	v_mfma_f32_16x16x32_bf16 v[10:13], v[152:155], v[212:215], v[10:13]
	v_mfma_f32_16x16x32_bf16 v[14:17], v[160:163], v[212:215], v[14:17]
	v_mfma_f32_16x16x32_bf16 v[50:53], v[164:167], v[180:183], v[50:53]
	v_mfma_f32_16x16x32_bf16 v[54:57], v[172:175], v[180:183], v[54:57]
	v_mfma_f32_16x16x32_bf16 v[34:37], v[164:167], v[188:191], v[34:37]
	v_mfma_f32_16x16x32_bf16 v[38:41], v[172:175], v[188:191], v[38:41]
	v_mfma_f32_16x16x32_bf16 v[18:21], v[164:167], v[196:199], v[18:21]
	v_mfma_f32_16x16x32_bf16 v[22:25], v[172:175], v[196:199], v[22:25]
	v_mfma_f32_16x16x32_bf16 v[6:9], v[164:167], v[208:211], v[6:9]
	v_mfma_f32_16x16x32_bf16 v[2:5], v[172:175], v[208:211], v[2:5]
	v_mfma_f32_16x16x32_bf16 v[50:53], v[168:171], v[184:187], v[50:53]
	v_mfma_f32_16x16x32_bf16 v[54:57], v[176:179], v[184:187], v[54:57]
	v_mfma_f32_16x16x32_bf16 v[34:37], v[168:171], v[192:195], v[34:37]
	v_mfma_f32_16x16x32_bf16 v[38:41], v[176:179], v[192:195], v[38:41]
	v_mfma_f32_16x16x32_bf16 v[18:21], v[168:171], v[204:207], v[18:21]
	v_mfma_f32_16x16x32_bf16 v[22:25], v[176:179], v[204:207], v[22:25]
	v_mfma_f32_16x16x32_bf16 v[6:9], v[168:171], v[212:215], v[6:9]
	v_mfma_f32_16x16x32_bf16 v[2:5], v[176:179], v[212:215], v[2:5]
	s_barrier
	s_setprio 0
	s_add_i32 s83, s83, 2
	s_add_u32 s58, s58, 0x100
	s_addc_u32 s59, s59, 0
	s_add_u32 s47, s47, 0x100
	s_addc_u32 s49, s49, 0
	s_cmp_gt_u32 s83, 5
	s_cbranch_scc0 .LBB0_927
	s_and_b64 vcc, exec, s[24:25]
	s_cbranch_vccz .LBB0_930
	s_barrier
